# c2pvq consumer loop: weight al(k+2) loaded after MFMA 8, ah(k+1) at block head (deeper prefetch, no extra regs); proj preload; conv1 hand-written epilogue
# baseline (speedup 1.0000x reference)
.LBB4_80:
	s_or_b64 exec, exec, s[0:1]
	s_lshl_b32 s6, s3, 2
	s_waitcnt lgkmcnt(0)
	s_barrier
	s_waitcnt vmcnt(20)
	ds_read_b128 v[138:141], v1 offset:10400
	s_waitcnt vmcnt(18)
	ds_read_b128 v[142:145], v1 offset:10416
	ds_read_b128 v[146:149], v1
	ds_read_b128 v[150:153], v1 offset:16
	s_waitcnt vmcnt(16) lgkmcnt(1)
	v_mfma_f32_32x32x16_f16 v[50:65], v[134:137], v[146:149], v[50:65]
	s_waitcnt lgkmcnt(0)
	v_mfma_f32_32x32x16_f16 v[50:65], v[130:133], v[150:153], v[50:65]
	v_mfma_f32_32x32x16_f16 v[50:65], v[130:133], v[146:149], v[50:65]
	ds_read_b128 v[146:149], v1 offset:20800
	ds_read_b128 v[150:153], v1 offset:20816
	v_mfma_f32_32x32x16_f16 v[34:49], v[134:137], v[138:141], v[34:49]
	v_mfma_f32_32x32x16_f16 v[34:49], v[130:133], v[142:145], v[34:49]
	v_mfma_f32_32x32x16_f16 v[34:49], v[130:133], v[138:141], v[34:49]
	ds_read_b128 v[138:141], v1 offset:31200
	ds_read_b128 v[142:145], v1 offset:31216
	s_waitcnt lgkmcnt(3)
	v_mfma_f32_32x32x16_f16 v[18:33], v[134:137], v[146:149], v[18:33]
	s_waitcnt lgkmcnt(2)
	v_mfma_f32_32x32x16_f16 v[18:33], v[130:133], v[150:153], v[18:33]
	v_mfma_f32_32x32x16_f16 v[18:33], v[130:133], v[146:149], v[18:33]
	ds_read_b128 v[146:149], v1 offset:2640
	ds_read_b128 v[150:153], v1 offset:2656
	s_waitcnt lgkmcnt(3)
	v_mfma_f32_32x32x16_f16 v[2:17], v[134:137], v[138:141], v[2:17]
	s_waitcnt lgkmcnt(2)
	v_mfma_f32_32x32x16_f16 v[2:17], v[130:133], v[142:145], v[2:17]
	v_mfma_f32_32x32x16_f16 v[2:17], v[130:133], v[138:141], v[2:17]
	ds_read_b128 v[130:133], v1 offset:13040
	ds_read_b128 v[134:137], v1 offset:13056
	s_waitcnt vmcnt(14) lgkmcnt(3)
	v_mfma_f32_32x32x16_f16 v[50:65], v[126:129], v[146:149], v[50:65]
	s_waitcnt lgkmcnt(2)
	v_mfma_f32_32x32x16_f16 v[50:65], v[122:125], v[150:153], v[50:65]
	v_mfma_f32_32x32x16_f16 v[50:65], v[122:125], v[146:149], v[50:65]
	ds_read_b128 v[138:141], v1 offset:23440
	ds_read_b128 v[142:145], v1 offset:23456
	s_waitcnt lgkmcnt(3)
	v_mfma_f32_32x32x16_f16 v[34:49], v[126:129], v[130:133], v[34:49]
	s_waitcnt lgkmcnt(2)
	v_mfma_f32_32x32x16_f16 v[34:49], v[122:125], v[134:137], v[34:49]
	v_mfma_f32_32x32x16_f16 v[34:49], v[122:125], v[130:133], v[34:49]
	ds_read_b128 v[130:133], v1 offset:33840
	ds_read_b128 v[134:137], v1 offset:33856
	s_waitcnt lgkmcnt(3)
	v_mfma_f32_32x32x16_f16 v[18:33], v[126:129], v[138:141], v[18:33]
	s_waitcnt lgkmcnt(2)
	v_mfma_f32_32x32x16_f16 v[18:33], v[122:125], v[142:145], v[18:33]
	v_mfma_f32_32x32x16_f16 v[18:33], v[122:125], v[138:141], v[18:33]
	ds_read_b128 v[138:141], v1 offset:80
	ds_read_b128 v[142:145], v1 offset:96
	s_waitcnt lgkmcnt(3)
	v_mfma_f32_32x32x16_f16 v[2:17], v[126:129], v[130:133], v[2:17]
	s_waitcnt lgkmcnt(2)
	v_mfma_f32_32x32x16_f16 v[2:17], v[122:125], v[134:137], v[2:17]
	v_mfma_f32_32x32x16_f16 v[2:17], v[122:125], v[130:133], v[2:17]
	ds_read_b128 v[122:125], v1 offset:10480
	ds_read_b128 v[126:129], v1 offset:10496
	s_waitcnt vmcnt(12) lgkmcnt(3)
	v_mfma_f32_32x32x16_f16 v[50:65], v[118:121], v[138:141], v[50:65]
	s_waitcnt lgkmcnt(2)
	v_mfma_f32_32x32x16_f16 v[50:65], v[114:117], v[142:145], v[50:65]
	v_mfma_f32_32x32x16_f16 v[50:65], v[114:117], v[138:141], v[50:65]
	ds_read_b128 v[130:133], v1 offset:20880
	ds_read_b128 v[134:137], v1 offset:20896
	s_waitcnt lgkmcnt(3)
	v_mfma_f32_32x32x16_f16 v[34:49], v[118:121], v[122:125], v[34:49]
	s_waitcnt lgkmcnt(2)
	v_mfma_f32_32x32x16_f16 v[34:49], v[114:117], v[126:129], v[34:49]
	v_mfma_f32_32x32x16_f16 v[34:49], v[114:117], v[122:125], v[34:49]
	ds_read_b128 v[122:125], v1 offset:31280
	ds_read_b128 v[126:129], v1 offset:31296
	s_waitcnt lgkmcnt(3)
	v_mfma_f32_32x32x16_f16 v[18:33], v[118:121], v[130:133], v[18:33]
	s_waitcnt lgkmcnt(2)
	v_mfma_f32_32x32x16_f16 v[18:33], v[114:117], v[134:137], v[18:33]
	v_mfma_f32_32x32x16_f16 v[18:33], v[114:117], v[130:133], v[18:33]
	ds_read_b128 v[130:133], v1 offset:5200
	ds_read_b128 v[134:137], v1 offset:5216
	s_waitcnt lgkmcnt(3)
	v_mfma_f32_32x32x16_f16 v[2:17], v[118:121], v[122:125], v[2:17]
	s_waitcnt lgkmcnt(2)
	v_mfma_f32_32x32x16_f16 v[2:17], v[114:117], v[126:129], v[2:17]
	v_mfma_f32_32x32x16_f16 v[2:17], v[114:117], v[122:125], v[2:17]
	ds_read_b128 v[114:117], v1 offset:15600
	ds_read_b128 v[118:121], v1 offset:15616
	s_waitcnt vmcnt(10) lgkmcnt(3)
	v_mfma_f32_32x32x16_f16 v[50:65], v[110:113], v[130:133], v[50:65]
	s_waitcnt lgkmcnt(2)
	v_mfma_f32_32x32x16_f16 v[50:65], v[106:109], v[134:137], v[50:65]
	v_mfma_f32_32x32x16_f16 v[50:65], v[106:109], v[130:133], v[50:65]
	ds_read_b128 v[122:125], v1 offset:26000
	ds_read_b128 v[126:129], v1 offset:26016
	s_waitcnt lgkmcnt(3)
	v_mfma_f32_32x32x16_f16 v[34:49], v[110:113], v[114:117], v[34:49]
	s_waitcnt lgkmcnt(2)
	v_mfma_f32_32x32x16_f16 v[34:49], v[106:109], v[118:121], v[34:49]
	v_mfma_f32_32x32x16_f16 v[34:49], v[106:109], v[114:117], v[34:49]
	ds_read_b128 v[114:117], v1 offset:36400
	ds_read_b128 v[118:121], v1 offset:36416
	s_waitcnt lgkmcnt(3)
	v_mfma_f32_32x32x16_f16 v[18:33], v[110:113], v[122:125], v[18:33]
	s_waitcnt lgkmcnt(2)
	v_mfma_f32_32x32x16_f16 v[18:33], v[106:109], v[126:129], v[18:33]
	v_mfma_f32_32x32x16_f16 v[18:33], v[106:109], v[122:125], v[18:33]
	ds_read_b128 v[122:125], v1 offset:7840
	ds_read_b128 v[126:129], v1 offset:7856
	s_waitcnt lgkmcnt(3)
	v_mfma_f32_32x32x16_f16 v[2:17], v[110:113], v[114:117], v[2:17]
	s_waitcnt lgkmcnt(2)
	v_mfma_f32_32x32x16_f16 v[2:17], v[106:109], v[118:121], v[2:17]
	v_mfma_f32_32x32x16_f16 v[2:17], v[106:109], v[114:117], v[2:17]
	ds_read_b128 v[106:109], v1 offset:18240
	ds_read_b128 v[110:113], v1 offset:18256
	s_waitcnt vmcnt(8) lgkmcnt(3)
	v_mfma_f32_32x32x16_f16 v[50:65], v[102:105], v[122:125], v[50:65]
	s_waitcnt lgkmcnt(2)
	v_mfma_f32_32x32x16_f16 v[50:65], v[98:101], v[126:129], v[50:65]
	v_mfma_f32_32x32x16_f16 v[50:65], v[98:101], v[122:125], v[50:65]
	ds_read_b128 v[114:117], v1 offset:28640
	ds_read_b128 v[118:121], v1 offset:28656
	s_waitcnt lgkmcnt(3)
	v_mfma_f32_32x32x16_f16 v[34:49], v[102:105], v[106:109], v[34:49]
	s_waitcnt lgkmcnt(2)
	v_mfma_f32_32x32x16_f16 v[34:49], v[98:101], v[110:113], v[34:49]
	v_mfma_f32_32x32x16_f16 v[34:49], v[98:101], v[106:109], v[34:49]
	ds_read_b128 v[106:109], v1 offset:39040
	ds_read_b128 v[110:113], v1 offset:39056
	s_waitcnt lgkmcnt(3)
	v_mfma_f32_32x32x16_f16 v[18:33], v[102:105], v[114:117], v[18:33]
	s_waitcnt lgkmcnt(2)
	v_mfma_f32_32x32x16_f16 v[18:33], v[98:101], v[118:121], v[18:33]
	v_mfma_f32_32x32x16_f16 v[18:33], v[98:101], v[114:117], v[18:33]
	ds_read_b128 v[114:117], v1 offset:5280
	ds_read_b128 v[118:121], v1 offset:5296
	s_waitcnt lgkmcnt(3)
	v_mfma_f32_32x32x16_f16 v[2:17], v[102:105], v[106:109], v[2:17]
	s_waitcnt lgkmcnt(2)
	v_mfma_f32_32x32x16_f16 v[2:17], v[98:101], v[110:113], v[2:17]
	v_mfma_f32_32x32x16_f16 v[2:17], v[98:101], v[106:109], v[2:17]
	ds_read_b128 v[98:101], v1 offset:15680
	ds_read_b128 v[102:105], v1 offset:15696
	s_waitcnt vmcnt(6) lgkmcnt(3)
	v_mfma_f32_32x32x16_f16 v[50:65], v[94:97], v[114:117], v[50:65]
	s_waitcnt lgkmcnt(2)
	v_mfma_f32_32x32x16_f16 v[50:65], v[90:93], v[118:121], v[50:65]
	v_mfma_f32_32x32x16_f16 v[50:65], v[90:93], v[114:117], v[50:65]
	ds_read_b128 v[106:109], v1 offset:26080
	ds_read_b128 v[110:113], v1 offset:26096
	s_waitcnt lgkmcnt(3)
	v_mfma_f32_32x32x16_f16 v[34:49], v[94:97], v[98:101], v[34:49]
	s_waitcnt lgkmcnt(2)
	v_mfma_f32_32x32x16_f16 v[34:49], v[90:93], v[102:105], v[34:49]
	v_mfma_f32_32x32x16_f16 v[34:49], v[90:93], v[98:101], v[34:49]
	ds_read_b128 v[98:101], v1 offset:36480
	ds_read_b128 v[102:105], v1 offset:36496
	s_waitcnt lgkmcnt(3)
	v_mfma_f32_32x32x16_f16 v[18:33], v[94:97], v[106:109], v[18:33]
	s_waitcnt lgkmcnt(2)
	v_mfma_f32_32x32x16_f16 v[18:33], v[90:93], v[110:113], v[18:33]
	v_mfma_f32_32x32x16_f16 v[18:33], v[90:93], v[106:109], v[18:33]
	ds_read_b128 v[106:109], v1 offset:10400
	ds_read_b128 v[110:113], v1 offset:10416
	s_waitcnt lgkmcnt(3)
	v_mfma_f32_32x32x16_f16 v[2:17], v[94:97], v[98:101], v[2:17]
	s_waitcnt lgkmcnt(2)
	v_mfma_f32_32x32x16_f16 v[2:17], v[90:93], v[102:105], v[2:17]
	v_mfma_f32_32x32x16_f16 v[2:17], v[90:93], v[98:101], v[2:17]
	ds_read_b128 v[90:93], v1 offset:20800
	ds_read_b128 v[94:97], v1 offset:20816
	s_waitcnt vmcnt(4) lgkmcnt(3)
	v_mfma_f32_32x32x16_f16 v[50:65], v[86:89], v[106:109], v[50:65]
	s_waitcnt lgkmcnt(2)
	v_mfma_f32_32x32x16_f16 v[50:65], v[82:85], v[110:113], v[50:65]
	v_mfma_f32_32x32x16_f16 v[50:65], v[82:85], v[106:109], v[50:65]
	ds_read_b128 v[98:101], v1 offset:31200
	ds_read_b128 v[102:105], v1 offset:31216
	s_waitcnt lgkmcnt(3)
	v_mfma_f32_32x32x16_f16 v[34:49], v[86:89], v[90:93], v[34:49]
	s_waitcnt lgkmcnt(2)
	v_mfma_f32_32x32x16_f16 v[34:49], v[82:85], v[94:97], v[34:49]
	v_mfma_f32_32x32x16_f16 v[34:49], v[82:85], v[90:93], v[34:49]
	ds_read_b128 v[90:93], v1 offset:41600
	ds_read_b128 v[94:97], v1 offset:41616
	s_waitcnt lgkmcnt(3)
	v_mfma_f32_32x32x16_f16 v[18:33], v[86:89], v[98:101], v[18:33]
	s_waitcnt lgkmcnt(2)
	v_mfma_f32_32x32x16_f16 v[18:33], v[82:85], v[102:105], v[18:33]
	v_mfma_f32_32x32x16_f16 v[18:33], v[82:85], v[98:101], v[18:33]
	ds_read_b128 v[98:101], v1 offset:13040
	ds_read_b128 v[102:105], v1 offset:13056
	s_waitcnt lgkmcnt(3)
	v_mfma_f32_32x32x16_f16 v[2:17], v[86:89], v[90:93], v[2:17]
	s_waitcnt lgkmcnt(2)
	v_mfma_f32_32x32x16_f16 v[2:17], v[82:85], v[94:97], v[2:17]
	v_mfma_f32_32x32x16_f16 v[2:17], v[82:85], v[90:93], v[2:17]
	ds_read_b128 v[82:85], v1 offset:23440
	ds_read_b128 v[86:89], v1 offset:23456
	s_waitcnt vmcnt(2) lgkmcnt(3)
	v_mfma_f32_32x32x16_f16 v[50:65], v[78:81], v[98:101], v[50:65]
	s_waitcnt lgkmcnt(2)
	v_mfma_f32_32x32x16_f16 v[50:65], v[74:77], v[102:105], v[50:65]
	v_mfma_f32_32x32x16_f16 v[50:65], v[74:77], v[98:101], v[50:65]
	ds_read_b128 v[90:93], v1 offset:33840
	ds_read_b128 v[94:97], v1 offset:33856
	s_waitcnt lgkmcnt(3)
	v_mfma_f32_32x32x16_f16 v[34:49], v[78:81], v[82:85], v[34:49]
	s_waitcnt lgkmcnt(2)
	v_mfma_f32_32x32x16_f16 v[34:49], v[74:77], v[86:89], v[34:49]
	v_mfma_f32_32x32x16_f16 v[34:49], v[74:77], v[82:85], v[34:49]
	ds_read_b128 v[82:85], v1 offset:44240
	ds_read_b128 v[86:89], v1 offset:44256
	s_waitcnt lgkmcnt(3)
	v_mfma_f32_32x32x16_f16 v[18:33], v[78:81], v[90:93], v[18:33]
	s_waitcnt lgkmcnt(2)
	v_mfma_f32_32x32x16_f16 v[18:33], v[74:77], v[94:97], v[18:33]
	v_mfma_f32_32x32x16_f16 v[18:33], v[74:77], v[90:93], v[18:33]
	ds_read_b128 v[90:93], v1 offset:10480
	ds_read_b128 v[94:97], v1 offset:10496
	s_waitcnt lgkmcnt(3)
	v_mfma_f32_32x32x16_f16 v[2:17], v[78:81], v[82:85], v[2:17]
	s_waitcnt lgkmcnt(2)
	v_mfma_f32_32x32x16_f16 v[2:17], v[74:77], v[86:89], v[2:17]
	v_mfma_f32_32x32x16_f16 v[2:17], v[74:77], v[82:85], v[2:17]
	ds_read_b128 v[74:77], v1 offset:20880
	ds_read_b128 v[78:81], v1 offset:20896
	s_waitcnt vmcnt(0) lgkmcnt(3)
	v_mfma_f32_32x32x16_f16 v[50:65], v[70:73], v[90:93], v[50:65]
	s_waitcnt lgkmcnt(2)
	v_mfma_f32_32x32x16_f16 v[50:65], v[66:69], v[94:97], v[50:65]
	v_mfma_f32_32x32x16_f16 v[50:65], v[66:69], v[90:93], v[50:65]
	ds_read_b128 v[82:85], v1 offset:31280
	ds_read_b128 v[86:89], v1 offset:31296
	s_waitcnt lgkmcnt(3)
	v_mfma_f32_32x32x16_f16 v[34:49], v[70:73], v[74:77], v[34:49]
	s_waitcnt lgkmcnt(2)
	v_mfma_f32_32x32x16_f16 v[34:49], v[66:69], v[78:81], v[34:49]
	v_mfma_f32_32x32x16_f16 v[34:49], v[66:69], v[74:77], v[34:49]
	ds_read_b128 v[74:77], v1 offset:41680
	ds_read_b128 v[78:81], v1 offset:41696
	s_waitcnt lgkmcnt(3)
	v_mfma_f32_32x32x16_f16 v[18:33], v[70:73], v[82:85], v[18:33]
	s_waitcnt lgkmcnt(2)
	v_mfma_f32_32x32x16_f16 v[18:33], v[66:69], v[86:89], v[18:33]
	v_mfma_f32_32x32x16_f16 v[18:33], v[66:69], v[82:85], v[18:33]
	s_waitcnt lgkmcnt(1)
	v_mfma_f32_32x32x16_f16 v[2:17], v[70:73], v[74:77], v[2:17]
	s_waitcnt lgkmcnt(0)
	v_mfma_f32_32x32x16_f16 v[2:17], v[66:69], v[78:81], v[2:17]
	v_mfma_f32_32x32x16_f16 v[2:17], v[66:69], v[74:77], v[2:17]
	v_and_b32_e32 v151, 31, v0
	v_lshrrev_b32_e32 v66, 1, v0
	v_lshrrev_b32_e32 v67, 3, v0
	v_and_b32_e32 v66, 0x60, v66
	v_and_b32_e32 v67, 4, v67
	v_or_b32_e32 v66, v66, v67
	v_lshlrev_b32_e32 v66, 2, v66
	global_load_dwordx4 v[68:71], v66, s[14:15]
	global_load_dwordx4 v[72:75], v66, s[14:15] offset:32
	global_load_dwordx4 v[76:79], v66, s[14:15] offset:64
	global_load_dwordx4 v[80:83], v66, s[14:15] offset:96
	global_load_dwordx4 v[84:87], v66, s[14:15] offset:1024
	global_load_dwordx4 v[88:91], v66, s[14:15] offset:1056
	global_load_dwordx4 v[92:95], v66, s[14:15] offset:1088
	global_load_dwordx4 v[96:99], v66, s[14:15] offset:1120
	v_readfirstlane_b32 s24, v0
	v_lshlrev_b32_e32 v100, 5, v151
	v_lshl_add_u32 v100, v67, 2, v100
	v_lshl_or_b32 v101, s2, 5, v151
	v_cmp_eq_u32_e64 s[26:27], 0, v101
	s_lshr_b32 s24, s24, 6
	s_lshl_b32 s25, s4, 23
	s_lshl_b32 s24, s24, 21
	s_add_u32 s25, s25, s24
	s_lshl_b32 s24, s3, 14
	s_add_u32 s25, s25, s24
	s_lshl_b32 s24, s2, 10
	s_add_u32 s25, s25, s24
	s_add_u32 s22, s20, s25
	s_addc_u32 s23, s21, 0
	s_cmp_lg_u32 s3, 0
	s_cbranch_scc1 .Lc1e_inner
	global_load_dwordx4 v[118:121], v66, s[14:15] offset:512
	global_load_dwordx4 v[122:125], v66, s[14:15] offset:544
	global_load_dwordx4 v[126:129], v66, s[14:15] offset:576
	global_load_dwordx4 v[130:133], v66, s[14:15] offset:608
	global_load_dwordx4 v[134:137], v66, s[14:15] offset:1536
	global_load_dwordx4 v[138:141], v66, s[14:15] offset:1568
	global_load_dwordx4 v[142:145], v66, s[14:15] offset:1600
	global_load_dwordx4 v[146:149], v66, s[14:15] offset:1632
	s_waitcnt vmcnt(0)
	v_sub_f32_e32 v118, v68, v118
	v_sub_f32_e32 v150, v118, v84
	v_add_f32_e32 v150, v150, v134
	v_cndmask_b32_e64 v102, v118, v150, s[26:27]
	v_sub_f32_e32 v119, v69, v119
	v_sub_f32_e32 v150, v119, v85
	v_add_f32_e32 v150, v150, v135
	v_cndmask_b32_e64 v103, v119, v150, s[26:27]
	v_sub_f32_e32 v120, v70, v120
	v_sub_f32_e32 v150, v120, v86
	v_add_f32_e32 v150, v150, v136
	v_cndmask_b32_e64 v104, v120, v150, s[26:27]
	v_sub_f32_e32 v121, v71, v121
	v_sub_f32_e32 v150, v121, v87
	v_add_f32_e32 v150, v150, v137
	v_cndmask_b32_e64 v105, v121, v150, s[26:27]
	v_sub_f32_e32 v122, v72, v122
	v_sub_f32_e32 v150, v122, v88
	v_add_f32_e32 v150, v150, v138
	v_cndmask_b32_e64 v106, v122, v150, s[26:27]
	v_sub_f32_e32 v123, v73, v123
	v_sub_f32_e32 v150, v123, v89
	v_add_f32_e32 v150, v150, v139
	v_cndmask_b32_e64 v107, v123, v150, s[26:27]
	v_sub_f32_e32 v124, v74, v124
	v_sub_f32_e32 v150, v124, v90
	v_add_f32_e32 v150, v150, v140
	v_cndmask_b32_e64 v108, v124, v150, s[26:27]
	v_sub_f32_e32 v125, v75, v125
	v_sub_f32_e32 v150, v125, v91
	v_add_f32_e32 v150, v150, v141
	v_cndmask_b32_e64 v109, v125, v150, s[26:27]
	v_sub_f32_e32 v126, v76, v126
	v_sub_f32_e32 v150, v126, v92
	v_add_f32_e32 v150, v150, v142
	v_cndmask_b32_e64 v110, v126, v150, s[26:27]
	v_sub_f32_e32 v127, v77, v127
	v_sub_f32_e32 v150, v127, v93
	v_add_f32_e32 v150, v150, v143
	v_cndmask_b32_e64 v111, v127, v150, s[26:27]
	v_sub_f32_e32 v128, v78, v128
	v_sub_f32_e32 v150, v128, v94
	v_add_f32_e32 v150, v150, v144
	v_cndmask_b32_e64 v112, v128, v150, s[26:27]
	v_sub_f32_e32 v129, v79, v129
	v_sub_f32_e32 v150, v129, v95
	v_add_f32_e32 v150, v150, v145
	v_cndmask_b32_e64 v113, v129, v150, s[26:27]
	v_sub_f32_e32 v130, v80, v130
	v_sub_f32_e32 v150, v130, v96
	v_add_f32_e32 v150, v150, v146
	v_cndmask_b32_e64 v114, v130, v150, s[26:27]
	v_sub_f32_e32 v131, v81, v131
	v_sub_f32_e32 v150, v131, v97
	v_add_f32_e32 v150, v150, v147
	v_cndmask_b32_e64 v115, v131, v150, s[26:27]
	v_sub_f32_e32 v132, v82, v132
	v_sub_f32_e32 v150, v132, v98
	v_add_f32_e32 v150, v150, v148
	v_cndmask_b32_e64 v116, v132, v150, s[26:27]
	v_sub_f32_e32 v133, v83, v133
	v_sub_f32_e32 v150, v133, v99
	v_add_f32_e32 v150, v150, v149
	v_cndmask_b32_e64 v117, v133, v150, s[26:27]
	v_sub_f32_e32 v84, v68, v84
	v_cndmask_b32_e64 v84, v68, v84, s[26:27]
	v_sub_f32_e32 v85, v69, v85
	v_cndmask_b32_e64 v85, v69, v85, s[26:27]
	v_sub_f32_e32 v86, v70, v86
	v_cndmask_b32_e64 v86, v70, v86, s[26:27]
	v_sub_f32_e32 v87, v71, v87
	v_cndmask_b32_e64 v87, v71, v87, s[26:27]
	v_sub_f32_e32 v88, v72, v88
	v_cndmask_b32_e64 v88, v72, v88, s[26:27]
	v_sub_f32_e32 v89, v73, v89
	v_cndmask_b32_e64 v89, v73, v89, s[26:27]
	v_sub_f32_e32 v90, v74, v90
	v_cndmask_b32_e64 v90, v74, v90, s[26:27]
	v_sub_f32_e32 v91, v75, v91
	v_cndmask_b32_e64 v91, v75, v91, s[26:27]
	v_sub_f32_e32 v92, v76, v92
	v_cndmask_b32_e64 v92, v76, v92, s[26:27]
	v_sub_f32_e32 v93, v77, v93
	v_cndmask_b32_e64 v93, v77, v93, s[26:27]
	v_sub_f32_e32 v94, v78, v94
	v_cndmask_b32_e64 v94, v78, v94, s[26:27]
	v_sub_f32_e32 v95, v79, v95
	v_cndmask_b32_e64 v95, v79, v95, s[26:27]
	v_sub_f32_e32 v96, v80, v96
	v_cndmask_b32_e64 v96, v80, v96, s[26:27]
	v_sub_f32_e32 v97, v81, v97
	v_cndmask_b32_e64 v97, v81, v97, s[26:27]
	v_sub_f32_e32 v98, v82, v98
	v_cndmask_b32_e64 v98, v82, v98, s[26:27]
	v_sub_f32_e32 v99, v83, v99
	v_cndmask_b32_e64 v99, v83, v99, s[26:27]
	s_branch .Lc1e_store

_Z7k_c2pvqI3GeoILi128ELi16ELi3ELi2EEEvPKfPKDv8_DF16_S3_S6_S3_S6_S3_S3_PfS7_PiS7_ii:
	v_readfirstlane_b32 s33, v0
	v_and_b32_e32 v1, 63, v0
	s_lshr_b32 s5, s33, 6
	v_and_b32_e32 v150, 31, v0
	v_bfe_u32 v151, v0, 5, 1
	s_cmpk_lt_u32 s33, 0x100
	v_lshlrev_b32_e32 v146, 1, v1
	s_cbranch_scc0 .LBB5_4
	s_load_dwordx4 s[8:11], s[0:1], 0x8
	v_mov_b32_e32 v147, 0
	v_and_b32_e32 v152, 32, v0
	s_movk_i32 s6, 0x50
	v_lshlrev_b32_e32 v2, 5, v1
	v_mov_b32_e32 v3, v147
	v_mad_u32_u24 v153, v150, s6, v152
	s_mov_b32 s7, 0
	s_waitcnt lgkmcnt(0)
	v_lshl_add_u64 v[148:149], s[8:9], 0, v[2:3]
	s_lshl_b32 s6, s5, 12
	v_lshl_add_u64 v[2:3], v[148:149], 0, s[6:7]
	global_load_dwordx4 v[134:137], v[2:3], off offset:16
	global_load_dwordx4 v[142:145], v[2:3], off offset:2064
	global_load_dwordx4 v[130:133], v[2:3], off
	global_load_dwordx4 v[138:141], v[2:3], off offset:2048
	s_add_u32 s58, s6, 0x4000
	s_mov_b32 s59, 0
	v_lshl_add_u64 v[188:189], v[148:149], 0, s[58:59]
	global_load_dwordx4 v[180:183], v[188:189], off offset:16
	s_nop 0
	global_load_dwordx4 v[188:191], v[188:189], off offset:2064
	v_add_u32_e32 v154, 0x10810, v153
	v_add_u32_e32 v155, 0x10820, v153
	v_add_u32_e32 v156, 0x130b0, v153
	v_add_u32_e32 v157, 0x130c0, v153
	v_add_u32_e32 v158, 0x11260, v153
	v_add_u32_e32 v159, 0x11270, v153
	v_add_u32_e32 v160, 0x13b00, v153
	v_add_u32_e32 v161, 0x13b10, v153
	v_add_u32_e32 v162, 0x10860, v153
	v_add_u32_e32 v163, 0x10870, v153
	v_add_u32_e32 v164, 0x13100, v153
	v_add_u32_e32 v165, 0x13110, v153
	v_add_u32_e32 v166, 0x11cb0, v153
	v_add_u32_e32 v167, 0x11cc0, v153
	v_add_u32_e32 v168, 0x14550, v153
	v_add_u32_e32 v169, 0x14560, v153
	v_add_u32_e32 v170, 0x15950, v153
	v_add_u32_e32 v171, 0x15960, v153
	v_add_u32_e32 v172, 0x163a0, v153
	v_add_u32_e32 v173, 0x163b0, v153
	v_add_u32_e32 v174, 0x159a0, v153
	v_add_u32_e32 v175, 0x159b0, v153
	s_or_b32 s12, s6, 0x24000
	s_add_i32 s8, s6, 0x44000
	s_mov_b32 s13, -2
	s_mov_b32 s14, 9
	v_mov_b32_e32 v114, v147
	v_mov_b32_e32 v115, v147
	v_mov_b32_e32 v116, v147
	v_mov_b32_e32 v117, v147
	v_mov_b32_e32 v118, v147
	v_mov_b32_e32 v119, v147
	v_mov_b32_e32 v120, v147
	v_mov_b32_e32 v121, v147
	v_mov_b32_e32 v122, v147
	v_mov_b32_e32 v123, v147
	v_mov_b32_e32 v124, v147
	v_mov_b32_e32 v125, v147
	v_mov_b32_e32 v126, v147
	v_mov_b32_e32 v127, v147
	v_mov_b32_e32 v128, v147
	v_mov_b32_e32 v129, v147
	v_mov_b32_e32 v98, v147
	v_mov_b32_e32 v99, v147
	v_mov_b32_e32 v100, v147
	v_mov_b32_e32 v101, v147
	v_mov_b32_e32 v102, v147
	v_mov_b32_e32 v103, v147
	v_mov_b32_e32 v104, v147
	v_mov_b32_e32 v105, v147
	v_mov_b32_e32 v106, v147
	v_mov_b32_e32 v107, v147
	v_mov_b32_e32 v108, v147
	v_mov_b32_e32 v109, v147
	v_mov_b32_e32 v110, v147
	v_mov_b32_e32 v111, v147
	v_mov_b32_e32 v112, v147
	v_mov_b32_e32 v113, v147
	v_mov_b32_e32 v82, v147
	v_mov_b32_e32 v83, v147
	v_mov_b32_e32 v84, v147
	v_mov_b32_e32 v85, v147
	v_mov_b32_e32 v86, v147
	v_mov_b32_e32 v87, v147
	v_mov_b32_e32 v88, v147
	v_mov_b32_e32 v89, v147
	v_mov_b32_e32 v90, v147
	v_mov_b32_e32 v91, v147
	v_mov_b32_e32 v92, v147
	v_mov_b32_e32 v93, v147
	v_mov_b32_e32 v94, v147
	v_mov_b32_e32 v95, v147
	v_mov_b32_e32 v96, v147
	v_mov_b32_e32 v97, v147
	v_mov_b32_e32 v66, v147
	v_mov_b32_e32 v67, v147
	v_mov_b32_e32 v68, v147
	v_mov_b32_e32 v69, v147
	v_mov_b32_e32 v70, v147
	v_mov_b32_e32 v71, v147
	v_mov_b32_e32 v72, v147
	v_mov_b32_e32 v73, v147
	v_mov_b32_e32 v74, v147
	v_mov_b32_e32 v75, v147
	v_mov_b32_e32 v76, v147
	v_mov_b32_e32 v77, v147
	v_mov_b32_e32 v78, v147
	v_mov_b32_e32 v79, v147
	v_mov_b32_e32 v80, v147
	v_mov_b32_e32 v81, v147
	v_mov_b32_e32 v50, v147
	v_mov_b32_e32 v51, v147
	v_mov_b32_e32 v52, v147
	v_mov_b32_e32 v53, v147
	v_mov_b32_e32 v54, v147
	v_mov_b32_e32 v55, v147
	v_mov_b32_e32 v56, v147
	v_mov_b32_e32 v57, v147
	v_mov_b32_e32 v58, v147
	v_mov_b32_e32 v59, v147
	v_mov_b32_e32 v60, v147
	v_mov_b32_e32 v61, v147
	v_mov_b32_e32 v62, v147
	v_mov_b32_e32 v63, v147
	v_mov_b32_e32 v64, v147
	v_mov_b32_e32 v65, v147
	v_mov_b32_e32 v34, v147
	v_mov_b32_e32 v35, v147
	v_mov_b32_e32 v36, v147
	v_mov_b32_e32 v37, v147
	v_mov_b32_e32 v38, v147
	v_mov_b32_e32 v39, v147
	v_mov_b32_e32 v40, v147
	v_mov_b32_e32 v41, v147
	v_mov_b32_e32 v42, v147
	v_mov_b32_e32 v43, v147
	v_mov_b32_e32 v44, v147
	v_mov_b32_e32 v45, v147
	v_mov_b32_e32 v46, v147
	v_mov_b32_e32 v47, v147
	v_mov_b32_e32 v48, v147
	v_mov_b32_e32 v49, v147
	v_mov_b32_e32 v18, v147
	v_mov_b32_e32 v19, v147
	v_mov_b32_e32 v20, v147
	v_mov_b32_e32 v21, v147
	v_mov_b32_e32 v22, v147
	v_mov_b32_e32 v23, v147
	v_mov_b32_e32 v24, v147
	v_mov_b32_e32 v25, v147
	v_mov_b32_e32 v26, v147
	v_mov_b32_e32 v27, v147
	v_mov_b32_e32 v28, v147
	v_mov_b32_e32 v29, v147
	v_mov_b32_e32 v30, v147
	v_mov_b32_e32 v31, v147
	v_mov_b32_e32 v32, v147
	v_mov_b32_e32 v33, v147
	v_mov_b32_e32 v2, v147
	v_mov_b32_e32 v3, v147
	v_mov_b32_e32 v4, v147
	v_mov_b32_e32 v5, v147
	v_mov_b32_e32 v6, v147
	v_mov_b32_e32 v7, v147
	v_mov_b32_e32 v8, v147
	v_mov_b32_e32 v9, v147
	v_mov_b32_e32 v10, v147
	v_mov_b32_e32 v11, v147
	v_mov_b32_e32 v12, v147
	v_mov_b32_e32 v13, v147
	v_mov_b32_e32 v14, v147
	v_mov_b32_e32 v15, v147
	v_mov_b32_e32 v16, v147
	v_mov_b32_e32 v17, v147
	s_barrier
.LBB5_2:
	s_add_i32 s6, s8, 0xfffc0000
	v_lshl_add_u64 v[184:185], v[148:149], 0, s[6:7]
	global_load_dwordx4 v[176:179], v[184:185], off
	s_nop 0
	global_load_dwordx4 v[184:187], v[184:185], off offset:2048
	ds_read_b128 v[192:195], v153
	ds_read_b128 v[196:199], v153 offset:16
	ds_read_b128 v[200:203], v153 offset:10400
	ds_read_b128 v[204:207], v153 offset:10416
	ds_read_b128 v[208:211], v153 offset:20800
	ds_read_b128 v[212:215], v153 offset:20816
	ds_read_b128 v[216:219], v153 offset:31200
	ds_read_b128 v[220:223], v153 offset:31216
	ds_read_b128 v[224:227], v153 offset:2640
	ds_read_b128 v[228:231], v153 offset:2656
	ds_read_b128 v[232:235], v153 offset:13040
	ds_read_b128 v[236:239], v153 offset:13056
	ds_read_b128 v[240:243], v153 offset:23440
	ds_read_b128 v[244:247], v153 offset:23456
	ds_read_b128 v[248:251], v153 offset:33840
	ds_read_b128 v[252:255], v153 offset:33856
	s_waitcnt vmcnt(6) lgkmcnt(14)
	v_mfma_f32_32x32x16_f16 v[114:129], v[134:137], v[192:195], v[114:129]
	v_mfma_f32_32x32x16_f16 v[50:65], v[142:145], v[192:195], v[50:65]
	s_waitcnt lgkmcnt(13)
	v_mfma_f32_32x32x16_f16 v[98:113], v[134:137], v[200:203], v[98:113]
	v_mfma_f32_32x32x16_f16 v[34:49], v[142:145], v[200:203], v[34:49]
	s_waitcnt lgkmcnt(11)
	v_mfma_f32_32x32x16_f16 v[82:97], v[134:137], v[208:211], v[82:97]
	v_mfma_f32_32x32x16_f16 v[18:33], v[142:145], v[208:211], v[18:33]
	s_waitcnt lgkmcnt(9)
	v_mfma_f32_32x32x16_f16 v[66:81], v[134:137], v[216:219], v[66:81]
	v_mfma_f32_32x32x16_f16 v[2:17], v[142:145], v[216:219], v[2:17]
	s_add_i32 s6, s8, 0xfffc4000
	v_lshl_add_u64 v[142:143], v[148:149], 0, s[6:7]
	global_load_dwordx4 v[134:137], v[142:143], off offset:16
	s_nop 0
	global_load_dwordx4 v[142:145], v[142:143], off offset:2064
	s_waitcnt vmcnt(6)
	v_mfma_f32_32x32x16_f16 v[114:129], v[130:133], v[196:199], v[114:129]
	v_mfma_f32_32x32x16_f16 v[50:65], v[138:141], v[196:199], v[50:65]
	v_mfma_f32_32x32x16_f16 v[98:113], v[130:133], v[204:207], v[98:113]
	v_mfma_f32_32x32x16_f16 v[34:49], v[138:141], v[204:207], v[34:49]
	v_mfma_f32_32x32x16_f16 v[82:97], v[130:133], v[212:215], v[82:97]
	v_mfma_f32_32x32x16_f16 v[18:33], v[138:141], v[212:215], v[18:33]
	s_waitcnt lgkmcnt(8)
	v_mfma_f32_32x32x16_f16 v[66:81], v[130:133], v[220:223], v[66:81]
	v_mfma_f32_32x32x16_f16 v[2:17], v[138:141], v[220:223], v[2:17]
	v_mfma_f32_32x32x16_f16 v[114:129], v[130:133], v[192:195], v[114:129]
	v_mfma_f32_32x32x16_f16 v[50:65], v[138:141], v[192:195], v[50:65]
	v_mfma_f32_32x32x16_f16 v[98:113], v[130:133], v[200:203], v[98:113]
	v_mfma_f32_32x32x16_f16 v[34:49], v[138:141], v[200:203], v[34:49]
	v_mfma_f32_32x32x16_f16 v[82:97], v[130:133], v[208:211], v[82:97]
	v_mfma_f32_32x32x16_f16 v[18:33], v[138:141], v[208:211], v[18:33]
	v_mfma_f32_32x32x16_f16 v[66:81], v[130:133], v[216:219], v[66:81]
	v_mfma_f32_32x32x16_f16 v[2:17], v[138:141], v[216:219], v[2:17]
	s_add_i32 s6, s8, 0xfffc4000
	v_lshl_add_u64 v[138:139], v[148:149], 0, s[6:7]
	global_load_dwordx4 v[130:133], v[138:139], off
	s_nop 0
	global_load_dwordx4 v[138:141], v[138:139], off offset:2048
	ds_read_b128 v[192:195], v153 offset:80
	ds_read_b128 v[196:199], v153 offset:96
	ds_read_b128 v[200:203], v153 offset:10480
	ds_read_b128 v[204:207], v153 offset:10496
	ds_read_b128 v[208:211], v153 offset:20880
	ds_read_b128 v[212:215], v153 offset:20896
	ds_read_b128 v[216:219], v153 offset:31280
	ds_read_b128 v[220:223], v153 offset:31296
	s_waitcnt vmcnt(6) lgkmcnt(14)
	v_mfma_f32_32x32x16_f16 v[114:129], v[180:183], v[224:227], v[114:129]
	v_mfma_f32_32x32x16_f16 v[50:65], v[188:191], v[224:227], v[50:65]
	s_waitcnt lgkmcnt(13)
	v_mfma_f32_32x32x16_f16 v[98:113], v[180:183], v[232:235], v[98:113]
	v_mfma_f32_32x32x16_f16 v[34:49], v[188:191], v[232:235], v[34:49]
	s_waitcnt lgkmcnt(11)
	v_mfma_f32_32x32x16_f16 v[82:97], v[180:183], v[240:243], v[82:97]
	v_mfma_f32_32x32x16_f16 v[18:33], v[188:191], v[240:243], v[18:33]
	s_waitcnt lgkmcnt(9)
	v_mfma_f32_32x32x16_f16 v[66:81], v[180:183], v[248:251], v[66:81]
	v_mfma_f32_32x32x16_f16 v[2:17], v[188:191], v[248:251], v[2:17]
	s_add_i32 s6, s8, 0xfffc8000
	v_lshl_add_u64 v[188:189], v[148:149], 0, s[6:7]
	global_load_dwordx4 v[180:183], v[188:189], off offset:16
	s_nop 0
	global_load_dwordx4 v[188:191], v[188:189], off offset:2064
	s_waitcnt vmcnt(6)
	v_mfma_f32_32x32x16_f16 v[114:129], v[176:179], v[228:231], v[114:129]
	v_mfma_f32_32x32x16_f16 v[50:65], v[184:187], v[228:231], v[50:65]
	v_mfma_f32_32x32x16_f16 v[98:113], v[176:179], v[236:239], v[98:113]
	v_mfma_f32_32x32x16_f16 v[34:49], v[184:187], v[236:239], v[34:49]
	v_mfma_f32_32x32x16_f16 v[82:97], v[176:179], v[244:247], v[82:97]
	v_mfma_f32_32x32x16_f16 v[18:33], v[184:187], v[244:247], v[18:33]
	s_waitcnt lgkmcnt(8)
	v_mfma_f32_32x32x16_f16 v[66:81], v[176:179], v[252:255], v[66:81]
	v_mfma_f32_32x32x16_f16 v[2:17], v[184:187], v[252:255], v[2:17]
	v_mfma_f32_32x32x16_f16 v[114:129], v[176:179], v[224:227], v[114:129]
	v_mfma_f32_32x32x16_f16 v[50:65], v[184:187], v[224:227], v[50:65]
	v_mfma_f32_32x32x16_f16 v[98:113], v[176:179], v[232:235], v[98:113]
	v_mfma_f32_32x32x16_f16 v[34:49], v[184:187], v[232:235], v[34:49]
	v_mfma_f32_32x32x16_f16 v[82:97], v[176:179], v[240:243], v[82:97]
	v_mfma_f32_32x32x16_f16 v[18:33], v[184:187], v[240:243], v[18:33]
	v_mfma_f32_32x32x16_f16 v[66:81], v[176:179], v[248:251], v[66:81]
	v_mfma_f32_32x32x16_f16 v[2:17], v[184:187], v[248:251], v[2:17]
	s_add_i32 s6, s8, 0xfffc8000
	v_lshl_add_u64 v[184:185], v[148:149], 0, s[6:7]
	global_load_dwordx4 v[176:179], v[184:185], off
	s_nop 0
	global_load_dwordx4 v[184:187], v[184:185], off offset:2048
	ds_read_b128 v[224:227], v153 offset:5200
	ds_read_b128 v[228:231], v153 offset:5216
	ds_read_b128 v[232:235], v153 offset:15600
	ds_read_b128 v[236:239], v153 offset:15616
	ds_read_b128 v[240:243], v153 offset:26000
	ds_read_b128 v[244:247], v153 offset:26016
	ds_read_b128 v[248:251], v153 offset:36400
	ds_read_b128 v[252:255], v153 offset:36416
	s_waitcnt vmcnt(6) lgkmcnt(14)
	v_mfma_f32_32x32x16_f16 v[114:129], v[134:137], v[192:195], v[114:129]
	v_mfma_f32_32x32x16_f16 v[50:65], v[142:145], v[192:195], v[50:65]
	s_waitcnt lgkmcnt(13)
	v_mfma_f32_32x32x16_f16 v[98:113], v[134:137], v[200:203], v[98:113]
	v_mfma_f32_32x32x16_f16 v[34:49], v[142:145], v[200:203], v[34:49]
	s_waitcnt lgkmcnt(11)
	v_mfma_f32_32x32x16_f16 v[82:97], v[134:137], v[208:211], v[82:97]
	v_mfma_f32_32x32x16_f16 v[18:33], v[142:145], v[208:211], v[18:33]
	s_waitcnt lgkmcnt(9)
	v_mfma_f32_32x32x16_f16 v[66:81], v[134:137], v[216:219], v[66:81]
	v_mfma_f32_32x32x16_f16 v[2:17], v[142:145], v[216:219], v[2:17]
	s_add_i32 s6, s8, 0xfffcc000
	v_lshl_add_u64 v[142:143], v[148:149], 0, s[6:7]
	global_load_dwordx4 v[134:137], v[142:143], off offset:16
	s_nop 0
	global_load_dwordx4 v[142:145], v[142:143], off offset:2064
	s_waitcnt vmcnt(6)
	v_mfma_f32_32x32x16_f16 v[114:129], v[130:133], v[196:199], v[114:129]
	v_mfma_f32_32x32x16_f16 v[50:65], v[138:141], v[196:199], v[50:65]
	v_mfma_f32_32x32x16_f16 v[98:113], v[130:133], v[204:207], v[98:113]
	v_mfma_f32_32x32x16_f16 v[34:49], v[138:141], v[204:207], v[34:49]
	v_mfma_f32_32x32x16_f16 v[82:97], v[130:133], v[212:215], v[82:97]
	v_mfma_f32_32x32x16_f16 v[18:33], v[138:141], v[212:215], v[18:33]
	s_waitcnt lgkmcnt(8)
	v_mfma_f32_32x32x16_f16 v[66:81], v[130:133], v[220:223], v[66:81]
	v_mfma_f32_32x32x16_f16 v[2:17], v[138:141], v[220:223], v[2:17]
	v_mfma_f32_32x32x16_f16 v[114:129], v[130:133], v[192:195], v[114:129]
	v_mfma_f32_32x32x16_f16 v[50:65], v[138:141], v[192:195], v[50:65]
	v_mfma_f32_32x32x16_f16 v[98:113], v[130:133], v[200:203], v[98:113]
	v_mfma_f32_32x32x16_f16 v[34:49], v[138:141], v[200:203], v[34:49]
	v_mfma_f32_32x32x16_f16 v[82:97], v[130:133], v[208:211], v[82:97]
	v_mfma_f32_32x32x16_f16 v[18:33], v[138:141], v[208:211], v[18:33]
	v_mfma_f32_32x32x16_f16 v[66:81], v[130:133], v[216:219], v[66:81]
	v_mfma_f32_32x32x16_f16 v[2:17], v[138:141], v[216:219], v[2:17]
	s_add_i32 s6, s8, 0xfffcc000
	v_lshl_add_u64 v[138:139], v[148:149], 0, s[6:7]
	global_load_dwordx4 v[130:133], v[138:139], off
	s_nop 0
	global_load_dwordx4 v[138:141], v[138:139], off offset:2048
	ds_read_b128 v[192:195], v153 offset:7840
	ds_read_b128 v[196:199], v153 offset:7856
	ds_read_b128 v[200:203], v153 offset:18240
	ds_read_b128 v[204:207], v153 offset:18256
	ds_read_b128 v[208:211], v153 offset:28640
	ds_read_b128 v[212:215], v153 offset:28656
	ds_read_b128 v[216:219], v153 offset:39040
	ds_read_b128 v[220:223], v153 offset:39056
	s_waitcnt vmcnt(6) lgkmcnt(14)
	v_mfma_f32_32x32x16_f16 v[114:129], v[180:183], v[224:227], v[114:129]
	v_mfma_f32_32x32x16_f16 v[50:65], v[188:191], v[224:227], v[50:65]
	s_waitcnt lgkmcnt(13)
	v_mfma_f32_32x32x16_f16 v[98:113], v[180:183], v[232:235], v[98:113]
	v_mfma_f32_32x32x16_f16 v[34:49], v[188:191], v[232:235], v[34:49]
	s_waitcnt lgkmcnt(11)
	v_mfma_f32_32x32x16_f16 v[82:97], v[180:183], v[240:243], v[82:97]
	v_mfma_f32_32x32x16_f16 v[18:33], v[188:191], v[240:243], v[18:33]
	s_waitcnt lgkmcnt(9)
	v_mfma_f32_32x32x16_f16 v[66:81], v[180:183], v[248:251], v[66:81]
	v_mfma_f32_32x32x16_f16 v[2:17], v[188:191], v[248:251], v[2:17]
	s_add_i32 s6, s8, 0xfffd0000
	v_lshl_add_u64 v[188:189], v[148:149], 0, s[6:7]
	global_load_dwordx4 v[180:183], v[188:189], off offset:16
	s_nop 0
	global_load_dwordx4 v[188:191], v[188:189], off offset:2064
	s_waitcnt vmcnt(6)
	v_mfma_f32_32x32x16_f16 v[114:129], v[176:179], v[228:231], v[114:129]
	v_mfma_f32_32x32x16_f16 v[50:65], v[184:187], v[228:231], v[50:65]
	v_mfma_f32_32x32x16_f16 v[98:113], v[176:179], v[236:239], v[98:113]
	v_mfma_f32_32x32x16_f16 v[34:49], v[184:187], v[236:239], v[34:49]
	v_mfma_f32_32x32x16_f16 v[82:97], v[176:179], v[244:247], v[82:97]
	v_mfma_f32_32x32x16_f16 v[18:33], v[184:187], v[244:247], v[18:33]
	s_waitcnt lgkmcnt(8)
	v_mfma_f32_32x32x16_f16 v[66:81], v[176:179], v[252:255], v[66:81]
	v_mfma_f32_32x32x16_f16 v[2:17], v[184:187], v[252:255], v[2:17]
	v_mfma_f32_32x32x16_f16 v[114:129], v[176:179], v[224:227], v[114:129]
	v_mfma_f32_32x32x16_f16 v[50:65], v[184:187], v[224:227], v[50:65]
	v_mfma_f32_32x32x16_f16 v[98:113], v[176:179], v[232:235], v[98:113]
	v_mfma_f32_32x32x16_f16 v[34:49], v[184:187], v[232:235], v[34:49]
	v_mfma_f32_32x32x16_f16 v[82:97], v[176:179], v[240:243], v[82:97]
	v_mfma_f32_32x32x16_f16 v[18:33], v[184:187], v[240:243], v[18:33]
	v_mfma_f32_32x32x16_f16 v[66:81], v[176:179], v[248:251], v[66:81]
	v_mfma_f32_32x32x16_f16 v[2:17], v[184:187], v[248:251], v[2:17]
	s_add_i32 s6, s8, 0xfffd0000
	v_lshl_add_u64 v[184:185], v[148:149], 0, s[6:7]
	global_load_dwordx4 v[176:179], v[184:185], off
	s_nop 0
	global_load_dwordx4 v[184:187], v[184:185], off offset:2048
	ds_read_b128 v[224:227], v153 offset:5280
	ds_read_b128 v[228:231], v153 offset:5296
	ds_read_b128 v[232:235], v153 offset:15680
	ds_read_b128 v[236:239], v153 offset:15696
	ds_read_b128 v[240:243], v153 offset:26080
	ds_read_b128 v[244:247], v153 offset:26096
	ds_read_b128 v[248:251], v153 offset:36480
	ds_read_b128 v[252:255], v153 offset:36496
	s_waitcnt vmcnt(6) lgkmcnt(14)
	v_mfma_f32_32x32x16_f16 v[114:129], v[134:137], v[192:195], v[114:129]
	v_mfma_f32_32x32x16_f16 v[50:65], v[142:145], v[192:195], v[50:65]
	s_waitcnt lgkmcnt(13)
	v_mfma_f32_32x32x16_f16 v[98:113], v[134:137], v[200:203], v[98:113]
	v_mfma_f32_32x32x16_f16 v[34:49], v[142:145], v[200:203], v[34:49]
	s_waitcnt lgkmcnt(11)
	v_mfma_f32_32x32x16_f16 v[82:97], v[134:137], v[208:211], v[82:97]
	v_mfma_f32_32x32x16_f16 v[18:33], v[142:145], v[208:211], v[18:33]
	s_waitcnt lgkmcnt(9)
	v_mfma_f32_32x32x16_f16 v[66:81], v[134:137], v[216:219], v[66:81]
	v_mfma_f32_32x32x16_f16 v[2:17], v[142:145], v[216:219], v[2:17]
	s_add_i32 s6, s8, 0xfffd4000
	v_lshl_add_u64 v[142:143], v[148:149], 0, s[6:7]
	global_load_dwordx4 v[134:137], v[142:143], off offset:16
	s_nop 0
	global_load_dwordx4 v[142:145], v[142:143], off offset:2064
	s_waitcnt vmcnt(6)
	v_mfma_f32_32x32x16_f16 v[114:129], v[130:133], v[196:199], v[114:129]
	v_mfma_f32_32x32x16_f16 v[50:65], v[138:141], v[196:199], v[50:65]
	v_mfma_f32_32x32x16_f16 v[98:113], v[130:133], v[204:207], v[98:113]
	v_mfma_f32_32x32x16_f16 v[34:49], v[138:141], v[204:207], v[34:49]
	v_mfma_f32_32x32x16_f16 v[82:97], v[130:133], v[212:215], v[82:97]
	v_mfma_f32_32x32x16_f16 v[18:33], v[138:141], v[212:215], v[18:33]
	s_waitcnt lgkmcnt(8)
	v_mfma_f32_32x32x16_f16 v[66:81], v[130:133], v[220:223], v[66:81]
	v_mfma_f32_32x32x16_f16 v[2:17], v[138:141], v[220:223], v[2:17]
	v_mfma_f32_32x32x16_f16 v[114:129], v[130:133], v[192:195], v[114:129]
	v_mfma_f32_32x32x16_f16 v[50:65], v[138:141], v[192:195], v[50:65]
	v_mfma_f32_32x32x16_f16 v[98:113], v[130:133], v[200:203], v[98:113]
	v_mfma_f32_32x32x16_f16 v[34:49], v[138:141], v[200:203], v[34:49]
	v_mfma_f32_32x32x16_f16 v[82:97], v[130:133], v[208:211], v[82:97]
	v_mfma_f32_32x32x16_f16 v[18:33], v[138:141], v[208:211], v[18:33]
	v_mfma_f32_32x32x16_f16 v[66:81], v[130:133], v[216:219], v[66:81]
	v_mfma_f32_32x32x16_f16 v[2:17], v[138:141], v[216:219], v[2:17]
	s_add_i32 s6, s8, 0xfffd4000
	v_lshl_add_u64 v[138:139], v[148:149], 0, s[6:7]
	global_load_dwordx4 v[130:133], v[138:139], off
	s_nop 0
	global_load_dwordx4 v[138:141], v[138:139], off offset:2048
	ds_read_b128 v[192:195], v153 offset:10400
	ds_read_b128 v[196:199], v153 offset:10416
	ds_read_b128 v[200:203], v153 offset:20800
	ds_read_b128 v[204:207], v153 offset:20816
	ds_read_b128 v[208:211], v153 offset:31200
	ds_read_b128 v[212:215], v153 offset:31216
	ds_read_b128 v[216:219], v153 offset:41600
	ds_read_b128 v[220:223], v153 offset:41616
	s_waitcnt vmcnt(6) lgkmcnt(14)
	v_mfma_f32_32x32x16_f16 v[114:129], v[180:183], v[224:227], v[114:129]
	v_mfma_f32_32x32x16_f16 v[50:65], v[188:191], v[224:227], v[50:65]
	s_waitcnt lgkmcnt(13)
	v_mfma_f32_32x32x16_f16 v[98:113], v[180:183], v[232:235], v[98:113]
	v_mfma_f32_32x32x16_f16 v[34:49], v[188:191], v[232:235], v[34:49]
	s_waitcnt lgkmcnt(11)
	v_mfma_f32_32x32x16_f16 v[82:97], v[180:183], v[240:243], v[82:97]
	v_mfma_f32_32x32x16_f16 v[18:33], v[188:191], v[240:243], v[18:33]
	s_waitcnt lgkmcnt(9)
	v_mfma_f32_32x32x16_f16 v[66:81], v[180:183], v[248:251], v[66:81]
	v_mfma_f32_32x32x16_f16 v[2:17], v[188:191], v[248:251], v[2:17]
	s_add_i32 s6, s8, 0xfffd8000
	v_lshl_add_u64 v[188:189], v[148:149], 0, s[6:7]
	global_load_dwordx4 v[180:183], v[188:189], off offset:16
	s_nop 0
	global_load_dwordx4 v[188:191], v[188:189], off offset:2064
	s_waitcnt vmcnt(6)
	v_mfma_f32_32x32x16_f16 v[114:129], v[176:179], v[228:231], v[114:129]
	v_mfma_f32_32x32x16_f16 v[50:65], v[184:187], v[228:231], v[50:65]
	v_mfma_f32_32x32x16_f16 v[98:113], v[176:179], v[236:239], v[98:113]
	v_mfma_f32_32x32x16_f16 v[34:49], v[184:187], v[236:239], v[34:49]
	v_mfma_f32_32x32x16_f16 v[82:97], v[176:179], v[244:247], v[82:97]
	v_mfma_f32_32x32x16_f16 v[18:33], v[184:187], v[244:247], v[18:33]
	s_waitcnt lgkmcnt(8)
	v_mfma_f32_32x32x16_f16 v[66:81], v[176:179], v[252:255], v[66:81]
	v_mfma_f32_32x32x16_f16 v[2:17], v[184:187], v[252:255], v[2:17]
	v_mfma_f32_32x32x16_f16 v[114:129], v[176:179], v[224:227], v[114:129]
	v_mfma_f32_32x32x16_f16 v[50:65], v[184:187], v[224:227], v[50:65]
	v_mfma_f32_32x32x16_f16 v[98:113], v[176:179], v[232:235], v[98:113]
	v_mfma_f32_32x32x16_f16 v[34:49], v[184:187], v[232:235], v[34:49]
	v_mfma_f32_32x32x16_f16 v[82:97], v[176:179], v[240:243], v[82:97]
	v_mfma_f32_32x32x16_f16 v[18:33], v[184:187], v[240:243], v[18:33]
	v_mfma_f32_32x32x16_f16 v[66:81], v[176:179], v[248:251], v[66:81]
	v_mfma_f32_32x32x16_f16 v[2:17], v[184:187], v[248:251], v[2:17]
	s_add_i32 s6, s8, 0xfffd8000
	v_lshl_add_u64 v[184:185], v[148:149], 0, s[6:7]
	global_load_dwordx4 v[176:179], v[184:185], off
	s_nop 0
	global_load_dwordx4 v[184:187], v[184:185], off offset:2048
	ds_read_b128 v[224:227], v153 offset:13040
	ds_read_b128 v[228:231], v153 offset:13056
	ds_read_b128 v[232:235], v153 offset:23440
	ds_read_b128 v[236:239], v153 offset:23456
	ds_read_b128 v[240:243], v153 offset:33840
	ds_read_b128 v[244:247], v153 offset:33856
	ds_read_b128 v[248:251], v153 offset:44240
	ds_read_b128 v[252:255], v153 offset:44256
	s_waitcnt vmcnt(6) lgkmcnt(14)
	v_mfma_f32_32x32x16_f16 v[114:129], v[134:137], v[192:195], v[114:129]
	v_mfma_f32_32x32x16_f16 v[50:65], v[142:145], v[192:195], v[50:65]
	s_waitcnt lgkmcnt(13)
	v_mfma_f32_32x32x16_f16 v[98:113], v[134:137], v[200:203], v[98:113]
	v_mfma_f32_32x32x16_f16 v[34:49], v[142:145], v[200:203], v[34:49]
	s_waitcnt lgkmcnt(11)
	v_mfma_f32_32x32x16_f16 v[82:97], v[134:137], v[208:211], v[82:97]
	v_mfma_f32_32x32x16_f16 v[18:33], v[142:145], v[208:211], v[18:33]
	s_waitcnt lgkmcnt(9)
	v_mfma_f32_32x32x16_f16 v[66:81], v[134:137], v[216:219], v[66:81]
	v_mfma_f32_32x32x16_f16 v[2:17], v[142:145], v[216:219], v[2:17]
	s_add_i32 s6, s8, 0xfffdc000
	v_lshl_add_u64 v[142:143], v[148:149], 0, s[6:7]
	global_load_dwordx4 v[134:137], v[142:143], off offset:16
	s_nop 0
	global_load_dwordx4 v[142:145], v[142:143], off offset:2064
	s_waitcnt vmcnt(6)
	v_mfma_f32_32x32x16_f16 v[114:129], v[130:133], v[196:199], v[114:129]
	v_mfma_f32_32x32x16_f16 v[50:65], v[138:141], v[196:199], v[50:65]
	v_mfma_f32_32x32x16_f16 v[98:113], v[130:133], v[204:207], v[98:113]
	v_mfma_f32_32x32x16_f16 v[34:49], v[138:141], v[204:207], v[34:49]
	v_mfma_f32_32x32x16_f16 v[82:97], v[130:133], v[212:215], v[82:97]
	v_mfma_f32_32x32x16_f16 v[18:33], v[138:141], v[212:215], v[18:33]
	s_waitcnt lgkmcnt(8)
	v_mfma_f32_32x32x16_f16 v[66:81], v[130:133], v[220:223], v[66:81]
	v_mfma_f32_32x32x16_f16 v[2:17], v[138:141], v[220:223], v[2:17]
	v_mfma_f32_32x32x16_f16 v[114:129], v[130:133], v[192:195], v[114:129]
	v_mfma_f32_32x32x16_f16 v[50:65], v[138:141], v[192:195], v[50:65]
	v_mfma_f32_32x32x16_f16 v[98:113], v[130:133], v[200:203], v[98:113]
	v_mfma_f32_32x32x16_f16 v[34:49], v[138:141], v[200:203], v[34:49]
	v_mfma_f32_32x32x16_f16 v[82:97], v[130:133], v[208:211], v[82:97]
	v_mfma_f32_32x32x16_f16 v[18:33], v[138:141], v[208:211], v[18:33]
	v_mfma_f32_32x32x16_f16 v[66:81], v[130:133], v[216:219], v[66:81]
	v_mfma_f32_32x32x16_f16 v[2:17], v[138:141], v[216:219], v[2:17]
	s_add_i32 s6, s8, 0xfffdc000
	v_lshl_add_u64 v[138:139], v[148:149], 0, s[6:7]
	global_load_dwordx4 v[130:133], v[138:139], off
	s_nop 0
	global_load_dwordx4 v[138:141], v[138:139], off offset:2048
	ds_read_b128 v[192:195], v153 offset:10480
	ds_read_b128 v[196:199], v153 offset:10496
	ds_read_b128 v[200:203], v153 offset:20880
	ds_read_b128 v[204:207], v153 offset:20896
	ds_read_b128 v[208:211], v153 offset:31280
	ds_read_b128 v[212:215], v153 offset:31296
	ds_read_b128 v[216:219], v153 offset:41680
	ds_read_b128 v[220:223], v153 offset:41696
	s_waitcnt vmcnt(6) lgkmcnt(14)
	v_mfma_f32_32x32x16_f16 v[114:129], v[180:183], v[224:227], v[114:129]
	v_mfma_f32_32x32x16_f16 v[50:65], v[188:191], v[224:227], v[50:65]
	s_waitcnt lgkmcnt(13)
	v_mfma_f32_32x32x16_f16 v[98:113], v[180:183], v[232:235], v[98:113]
	v_mfma_f32_32x32x16_f16 v[34:49], v[188:191], v[232:235], v[34:49]
	s_waitcnt lgkmcnt(11)
	v_mfma_f32_32x32x16_f16 v[82:97], v[180:183], v[240:243], v[82:97]
	v_mfma_f32_32x32x16_f16 v[18:33], v[188:191], v[240:243], v[18:33]
	s_waitcnt lgkmcnt(9)
	v_mfma_f32_32x32x16_f16 v[66:81], v[180:183], v[248:251], v[66:81]
	v_mfma_f32_32x32x16_f16 v[2:17], v[188:191], v[248:251], v[2:17]
	s_add_i32 s6, s8, 0xfffe0000
	v_lshl_add_u64 v[188:189], v[148:149], 0, s[6:7]
	global_load_dwordx4 v[180:183], v[188:189], off offset:16
	s_nop 0
	global_load_dwordx4 v[188:191], v[188:189], off offset:2064
	s_waitcnt vmcnt(6)
	v_mfma_f32_32x32x16_f16 v[114:129], v[176:179], v[228:231], v[114:129]
	v_mfma_f32_32x32x16_f16 v[50:65], v[184:187], v[228:231], v[50:65]
	v_mfma_f32_32x32x16_f16 v[98:113], v[176:179], v[236:239], v[98:113]
	v_mfma_f32_32x32x16_f16 v[34:49], v[184:187], v[236:239], v[34:49]
	v_mfma_f32_32x32x16_f16 v[82:97], v[176:179], v[244:247], v[82:97]
	v_mfma_f32_32x32x16_f16 v[18:33], v[184:187], v[244:247], v[18:33]
	s_waitcnt lgkmcnt(8)
	v_mfma_f32_32x32x16_f16 v[66:81], v[176:179], v[252:255], v[66:81]
	v_mfma_f32_32x32x16_f16 v[2:17], v[184:187], v[252:255], v[2:17]
	v_mfma_f32_32x32x16_f16 v[114:129], v[176:179], v[224:227], v[114:129]
	v_mfma_f32_32x32x16_f16 v[50:65], v[184:187], v[224:227], v[50:65]
	v_mfma_f32_32x32x16_f16 v[98:113], v[176:179], v[232:235], v[98:113]
	v_mfma_f32_32x32x16_f16 v[34:49], v[184:187], v[232:235], v[34:49]
	v_mfma_f32_32x32x16_f16 v[82:97], v[176:179], v[240:243], v[82:97]
	v_mfma_f32_32x32x16_f16 v[18:33], v[184:187], v[240:243], v[18:33]
	v_mfma_f32_32x32x16_f16 v[66:81], v[176:179], v[248:251], v[66:81]
	v_mfma_f32_32x32x16_f16 v[2:17], v[184:187], v[248:251], v[2:17]
	s_add_i32 s6, s8, 0xfffe0000
	v_lshl_add_u64 v[184:185], v[148:149], 0, s[6:7]
	global_load_dwordx4 v[176:179], v[184:185], off
	s_nop 0
	global_load_dwordx4 v[184:187], v[184:185], off offset:2048
	s_waitcnt vmcnt(6) lgkmcnt(7)
	v_mfma_f32_32x32x16_f16 v[114:129], v[134:137], v[192:195], v[114:129]
	v_mfma_f32_32x32x16_f16 v[50:65], v[142:145], v[192:195], v[50:65]
	s_waitcnt lgkmcnt(5)
	v_mfma_f32_32x32x16_f16 v[98:113], v[134:137], v[200:203], v[98:113]
	v_mfma_f32_32x32x16_f16 v[34:49], v[142:145], v[200:203], v[34:49]
	s_waitcnt lgkmcnt(3)
	v_mfma_f32_32x32x16_f16 v[82:97], v[134:137], v[208:211], v[82:97]
	v_mfma_f32_32x32x16_f16 v[18:33], v[142:145], v[208:211], v[18:33]
	s_waitcnt lgkmcnt(1)
	v_mfma_f32_32x32x16_f16 v[66:81], v[134:137], v[216:219], v[66:81]
	v_mfma_f32_32x32x16_f16 v[2:17], v[142:145], v[216:219], v[2:17]
	s_add_i32 s6, s8, 0xfffe4000
	v_lshl_add_u64 v[142:143], v[148:149], 0, s[6:7]
	global_load_dwordx4 v[134:137], v[142:143], off offset:16
	s_nop 0
	global_load_dwordx4 v[142:145], v[142:143], off offset:2064
	s_waitcnt vmcnt(6)
	v_mfma_f32_32x32x16_f16 v[114:129], v[130:133], v[196:199], v[114:129]
	v_mfma_f32_32x32x16_f16 v[50:65], v[138:141], v[196:199], v[50:65]
	v_mfma_f32_32x32x16_f16 v[98:113], v[130:133], v[204:207], v[98:113]
	v_mfma_f32_32x32x16_f16 v[34:49], v[138:141], v[204:207], v[34:49]
	v_mfma_f32_32x32x16_f16 v[82:97], v[130:133], v[212:215], v[82:97]
	v_mfma_f32_32x32x16_f16 v[18:33], v[138:141], v[212:215], v[18:33]
	s_waitcnt lgkmcnt(0)
	v_mfma_f32_32x32x16_f16 v[66:81], v[130:133], v[220:223], v[66:81]
	v_mfma_f32_32x32x16_f16 v[2:17], v[138:141], v[220:223], v[2:17]
	v_mfma_f32_32x32x16_f16 v[114:129], v[130:133], v[192:195], v[114:129]
	v_mfma_f32_32x32x16_f16 v[50:65], v[138:141], v[192:195], v[50:65]
	v_mfma_f32_32x32x16_f16 v[98:113], v[130:133], v[200:203], v[98:113]
	v_mfma_f32_32x32x16_f16 v[34:49], v[138:141], v[200:203], v[34:49]
	v_mfma_f32_32x32x16_f16 v[82:97], v[130:133], v[208:211], v[82:97]
	v_mfma_f32_32x32x16_f16 v[18:33], v[138:141], v[208:211], v[18:33]
	v_mfma_f32_32x32x16_f16 v[66:81], v[130:133], v[216:219], v[66:81]
	v_mfma_f32_32x32x16_f16 v[2:17], v[138:141], v[216:219], v[2:17]
	s_barrier
	s_add_i32 s6, s8, 0xfffe4000
	v_lshl_add_u64 v[138:139], v[148:149], 0, s[6:7]
	global_load_dwordx4 v[130:133], v[138:139], off
	s_nop 0
	global_load_dwordx4 v[138:141], v[138:139], off offset:2048
	ds_read_b128 v[192:195], v153 offset:46800
	ds_read_b128 v[196:199], v153 offset:46816
	ds_read_b128 v[200:203], v153 offset:57200
	ds_read_b128 v[204:207], v153 offset:57216
	ds_read_b128 v[208:211], v154
	ds_read_b128 v[212:215], v155
	ds_read_b128 v[216:219], v156
	ds_read_b128 v[220:223], v157
	ds_read_b128 v[224:227], v153 offset:49440
	ds_read_b128 v[228:231], v153 offset:49456
	ds_read_b128 v[232:235], v153 offset:59840
	ds_read_b128 v[236:239], v153 offset:59856
	ds_read_b128 v[240:243], v158
	ds_read_b128 v[244:247], v159
	ds_read_b128 v[248:251], v160
	ds_read_b128 v[252:255], v161
	s_waitcnt vmcnt(6) lgkmcnt(14)
	v_mfma_f32_32x32x16_f16 v[114:129], v[180:183], v[192:195], v[114:129]
	v_mfma_f32_32x32x16_f16 v[50:65], v[188:191], v[192:195], v[50:65]
	s_waitcnt lgkmcnt(13)
	v_mfma_f32_32x32x16_f16 v[98:113], v[180:183], v[200:203], v[98:113]
	v_mfma_f32_32x32x16_f16 v[34:49], v[188:191], v[200:203], v[34:49]
	s_waitcnt lgkmcnt(11)
	v_mfma_f32_32x32x16_f16 v[82:97], v[180:183], v[208:211], v[82:97]
	v_mfma_f32_32x32x16_f16 v[18:33], v[188:191], v[208:211], v[18:33]
	s_waitcnt lgkmcnt(9)
	v_mfma_f32_32x32x16_f16 v[66:81], v[180:183], v[216:219], v[66:81]
	v_mfma_f32_32x32x16_f16 v[2:17], v[188:191], v[216:219], v[2:17]
	s_add_i32 s6, s8, 0xfffe8000
	v_lshl_add_u64 v[188:189], v[148:149], 0, s[6:7]
	global_load_dwordx4 v[180:183], v[188:189], off offset:16
	s_nop 0
	global_load_dwordx4 v[188:191], v[188:189], off offset:2064
	s_waitcnt vmcnt(6)
	v_mfma_f32_32x32x16_f16 v[114:129], v[176:179], v[196:199], v[114:129]
	v_mfma_f32_32x32x16_f16 v[50:65], v[184:187], v[196:199], v[50:65]
	v_mfma_f32_32x32x16_f16 v[98:113], v[176:179], v[204:207], v[98:113]
	v_mfma_f32_32x32x16_f16 v[34:49], v[184:187], v[204:207], v[34:49]
	v_mfma_f32_32x32x16_f16 v[82:97], v[176:179], v[212:215], v[82:97]
	v_mfma_f32_32x32x16_f16 v[18:33], v[184:187], v[212:215], v[18:33]
	s_waitcnt lgkmcnt(8)
	v_mfma_f32_32x32x16_f16 v[66:81], v[176:179], v[220:223], v[66:81]
	v_mfma_f32_32x32x16_f16 v[2:17], v[184:187], v[220:223], v[2:17]
	v_mfma_f32_32x32x16_f16 v[114:129], v[176:179], v[192:195], v[114:129]
	v_mfma_f32_32x32x16_f16 v[50:65], v[184:187], v[192:195], v[50:65]
	v_mfma_f32_32x32x16_f16 v[98:113], v[176:179], v[200:203], v[98:113]
	v_mfma_f32_32x32x16_f16 v[34:49], v[184:187], v[200:203], v[34:49]
	v_mfma_f32_32x32x16_f16 v[82:97], v[176:179], v[208:211], v[82:97]
	v_mfma_f32_32x32x16_f16 v[18:33], v[184:187], v[208:211], v[18:33]
	v_mfma_f32_32x32x16_f16 v[66:81], v[176:179], v[216:219], v[66:81]
	v_mfma_f32_32x32x16_f16 v[2:17], v[184:187], v[216:219], v[2:17]
	s_add_i32 s6, s8, 0xfffe8000
	v_lshl_add_u64 v[184:185], v[148:149], 0, s[6:7]
	global_load_dwordx4 v[176:179], v[184:185], off
	s_nop 0
	global_load_dwordx4 v[184:187], v[184:185], off offset:2048
	ds_read_b128 v[192:195], v153 offset:46880
	ds_read_b128 v[196:199], v153 offset:46896
	ds_read_b128 v[200:203], v153 offset:57280
	ds_read_b128 v[204:207], v153 offset:57296
	ds_read_b128 v[208:211], v162
	ds_read_b128 v[212:215], v163
	ds_read_b128 v[216:219], v164
	ds_read_b128 v[220:223], v165
	s_waitcnt vmcnt(6) lgkmcnt(14)
	v_mfma_f32_32x32x16_f16 v[114:129], v[134:137], v[224:227], v[114:129]
	v_mfma_f32_32x32x16_f16 v[50:65], v[142:145], v[224:227], v[50:65]
	s_waitcnt lgkmcnt(13)
	v_mfma_f32_32x32x16_f16 v[98:113], v[134:137], v[232:235], v[98:113]
	v_mfma_f32_32x32x16_f16 v[34:49], v[142:145], v[232:235], v[34:49]
	s_waitcnt lgkmcnt(11)
	v_mfma_f32_32x32x16_f16 v[82:97], v[134:137], v[240:243], v[82:97]
	v_mfma_f32_32x32x16_f16 v[18:33], v[142:145], v[240:243], v[18:33]
	s_waitcnt lgkmcnt(9)
	v_mfma_f32_32x32x16_f16 v[66:81], v[134:137], v[248:251], v[66:81]
	v_mfma_f32_32x32x16_f16 v[2:17], v[142:145], v[248:251], v[2:17]
	s_add_i32 s6, s8, 0xfffec000
	v_lshl_add_u64 v[142:143], v[148:149], 0, s[6:7]
	global_load_dwordx4 v[134:137], v[142:143], off offset:16
	s_nop 0
	global_load_dwordx4 v[142:145], v[142:143], off offset:2064
	s_waitcnt vmcnt(6)
	v_mfma_f32_32x32x16_f16 v[114:129], v[130:133], v[228:231], v[114:129]
	v_mfma_f32_32x32x16_f16 v[50:65], v[138:141], v[228:231], v[50:65]
	v_mfma_f32_32x32x16_f16 v[98:113], v[130:133], v[236:239], v[98:113]
	v_mfma_f32_32x32x16_f16 v[34:49], v[138:141], v[236:239], v[34:49]
	v_mfma_f32_32x32x16_f16 v[82:97], v[130:133], v[244:247], v[82:97]
	v_mfma_f32_32x32x16_f16 v[18:33], v[138:141], v[244:247], v[18:33]
	s_waitcnt lgkmcnt(8)
	v_mfma_f32_32x32x16_f16 v[66:81], v[130:133], v[252:255], v[66:81]
	v_mfma_f32_32x32x16_f16 v[2:17], v[138:141], v[252:255], v[2:17]
	v_mfma_f32_32x32x16_f16 v[114:129], v[130:133], v[224:227], v[114:129]
	v_mfma_f32_32x32x16_f16 v[50:65], v[138:141], v[224:227], v[50:65]
	v_mfma_f32_32x32x16_f16 v[98:113], v[130:133], v[232:235], v[98:113]
	v_mfma_f32_32x32x16_f16 v[34:49], v[138:141], v[232:235], v[34:49]
	v_mfma_f32_32x32x16_f16 v[82:97], v[130:133], v[240:243], v[82:97]
	v_mfma_f32_32x32x16_f16 v[18:33], v[138:141], v[240:243], v[18:33]
	v_mfma_f32_32x32x16_f16 v[66:81], v[130:133], v[248:251], v[66:81]
	v_mfma_f32_32x32x16_f16 v[2:17], v[138:141], v[248:251], v[2:17]
	s_add_i32 s6, s8, 0xfffec000
	v_lshl_add_u64 v[138:139], v[148:149], 0, s[6:7]
	global_load_dwordx4 v[130:133], v[138:139], off
	s_nop 0
	global_load_dwordx4 v[138:141], v[138:139], off offset:2048
	ds_read_b128 v[224:227], v153 offset:52000
	ds_read_b128 v[228:231], v153 offset:52016
	ds_read_b128 v[232:235], v153 offset:62400
	ds_read_b128 v[236:239], v153 offset:62416
	v_add_u32_e32 v240, 0x11c60, v153
	v_add_u32_e32 v244, 0x11c70, v153
	v_add_u32_e32 v248, 0x14500, v153
	v_add_u32_e32 v252, 0x14510, v153
	ds_read_b128 v[240:243], v240
	ds_read_b128 v[244:247], v244
	ds_read_b128 v[248:251], v248
	ds_read_b128 v[252:255], v252
	s_waitcnt vmcnt(6) lgkmcnt(14)
	v_mfma_f32_32x32x16_f16 v[114:129], v[180:183], v[192:195], v[114:129]
	v_mfma_f32_32x32x16_f16 v[50:65], v[188:191], v[192:195], v[50:65]
	s_waitcnt lgkmcnt(13)
	v_mfma_f32_32x32x16_f16 v[98:113], v[180:183], v[200:203], v[98:113]
	v_mfma_f32_32x32x16_f16 v[34:49], v[188:191], v[200:203], v[34:49]
	s_waitcnt lgkmcnt(11)
	v_mfma_f32_32x32x16_f16 v[82:97], v[180:183], v[208:211], v[82:97]
	v_mfma_f32_32x32x16_f16 v[18:33], v[188:191], v[208:211], v[18:33]
	s_waitcnt lgkmcnt(9)
	v_mfma_f32_32x32x16_f16 v[66:81], v[180:183], v[216:219], v[66:81]
	v_mfma_f32_32x32x16_f16 v[2:17], v[188:191], v[216:219], v[2:17]
	s_add_i32 s6, s8, 0xffff0000
	v_lshl_add_u64 v[188:189], v[148:149], 0, s[6:7]
	global_load_dwordx4 v[180:183], v[188:189], off offset:16
	s_nop 0
	global_load_dwordx4 v[188:191], v[188:189], off offset:2064
	s_waitcnt vmcnt(6)
	v_mfma_f32_32x32x16_f16 v[114:129], v[176:179], v[196:199], v[114:129]
	v_mfma_f32_32x32x16_f16 v[50:65], v[184:187], v[196:199], v[50:65]
	v_mfma_f32_32x32x16_f16 v[98:113], v[176:179], v[204:207], v[98:113]
	v_mfma_f32_32x32x16_f16 v[34:49], v[184:187], v[204:207], v[34:49]
	v_mfma_f32_32x32x16_f16 v[82:97], v[176:179], v[212:215], v[82:97]
	v_mfma_f32_32x32x16_f16 v[18:33], v[184:187], v[212:215], v[18:33]
	s_waitcnt lgkmcnt(8)
	v_mfma_f32_32x32x16_f16 v[66:81], v[176:179], v[220:223], v[66:81]
	v_mfma_f32_32x32x16_f16 v[2:17], v[184:187], v[220:223], v[2:17]
	v_mfma_f32_32x32x16_f16 v[114:129], v[176:179], v[192:195], v[114:129]
	v_mfma_f32_32x32x16_f16 v[50:65], v[184:187], v[192:195], v[50:65]
	v_mfma_f32_32x32x16_f16 v[98:113], v[176:179], v[200:203], v[98:113]
	v_mfma_f32_32x32x16_f16 v[34:49], v[184:187], v[200:203], v[34:49]
	v_mfma_f32_32x32x16_f16 v[82:97], v[176:179], v[208:211], v[82:97]
	v_mfma_f32_32x32x16_f16 v[18:33], v[184:187], v[208:211], v[18:33]
	v_mfma_f32_32x32x16_f16 v[66:81], v[176:179], v[216:219], v[66:81]
	v_mfma_f32_32x32x16_f16 v[2:17], v[184:187], v[216:219], v[2:17]
	s_add_i32 s6, s8, 0xffff0000
	v_lshl_add_u64 v[184:185], v[148:149], 0, s[6:7]
	global_load_dwordx4 v[176:179], v[184:185], off
	s_nop 0
	global_load_dwordx4 v[184:187], v[184:185], off offset:2048
	ds_read_b128 v[192:195], v153 offset:54640
	ds_read_b128 v[196:199], v153 offset:54656
	ds_read_b128 v[200:203], v153 offset:65040
	ds_read_b128 v[204:207], v153 offset:65056
	v_add_u32_e32 v208, 0x126b0, v153
	v_add_u32_e32 v212, 0x126c0, v153
	v_add_u32_e32 v216, 0x14f50, v153
	v_add_u32_e32 v220, 0x14f60, v153
	ds_read_b128 v[208:211], v208
	ds_read_b128 v[212:215], v212
	ds_read_b128 v[216:219], v216
	ds_read_b128 v[220:223], v220
	s_waitcnt vmcnt(6) lgkmcnt(14)
	v_mfma_f32_32x32x16_f16 v[114:129], v[134:137], v[224:227], v[114:129]
	v_mfma_f32_32x32x16_f16 v[50:65], v[142:145], v[224:227], v[50:65]
	s_waitcnt lgkmcnt(13)
	v_mfma_f32_32x32x16_f16 v[98:113], v[134:137], v[232:235], v[98:113]
	v_mfma_f32_32x32x16_f16 v[34:49], v[142:145], v[232:235], v[34:49]
	s_waitcnt lgkmcnt(11)
	v_mfma_f32_32x32x16_f16 v[82:97], v[134:137], v[240:243], v[82:97]
	v_mfma_f32_32x32x16_f16 v[18:33], v[142:145], v[240:243], v[18:33]
	s_waitcnt lgkmcnt(9)
	v_mfma_f32_32x32x16_f16 v[66:81], v[134:137], v[248:251], v[66:81]
	v_mfma_f32_32x32x16_f16 v[2:17], v[142:145], v[248:251], v[2:17]
	s_add_i32 s6, s8, 0xffff4000
	v_lshl_add_u64 v[142:143], v[148:149], 0, s[6:7]
	global_load_dwordx4 v[134:137], v[142:143], off offset:16
	s_nop 0
	global_load_dwordx4 v[142:145], v[142:143], off offset:2064
	s_waitcnt vmcnt(6)
	v_mfma_f32_32x32x16_f16 v[114:129], v[130:133], v[228:231], v[114:129]
	v_mfma_f32_32x32x16_f16 v[50:65], v[138:141], v[228:231], v[50:65]
	v_mfma_f32_32x32x16_f16 v[98:113], v[130:133], v[236:239], v[98:113]
	v_mfma_f32_32x32x16_f16 v[34:49], v[138:141], v[236:239], v[34:49]
	v_mfma_f32_32x32x16_f16 v[82:97], v[130:133], v[244:247], v[82:97]
	v_mfma_f32_32x32x16_f16 v[18:33], v[138:141], v[244:247], v[18:33]
	s_waitcnt lgkmcnt(8)
	v_mfma_f32_32x32x16_f16 v[66:81], v[130:133], v[252:255], v[66:81]
	v_mfma_f32_32x32x16_f16 v[2:17], v[138:141], v[252:255], v[2:17]
	v_mfma_f32_32x32x16_f16 v[114:129], v[130:133], v[224:227], v[114:129]
	v_mfma_f32_32x32x16_f16 v[50:65], v[138:141], v[224:227], v[50:65]
	v_mfma_f32_32x32x16_f16 v[98:113], v[130:133], v[232:235], v[98:113]
	v_mfma_f32_32x32x16_f16 v[34:49], v[138:141], v[232:235], v[34:49]
	v_mfma_f32_32x32x16_f16 v[82:97], v[130:133], v[240:243], v[82:97]
	v_mfma_f32_32x32x16_f16 v[18:33], v[138:141], v[240:243], v[18:33]
	v_mfma_f32_32x32x16_f16 v[66:81], v[130:133], v[248:251], v[66:81]
	v_mfma_f32_32x32x16_f16 v[2:17], v[138:141], v[248:251], v[2:17]
	s_add_i32 s6, s8, 0xffff4000
	v_lshl_add_u64 v[138:139], v[148:149], 0, s[6:7]
	global_load_dwordx4 v[130:133], v[138:139], off
	s_nop 0
	global_load_dwordx4 v[138:141], v[138:139], off offset:2048
	ds_read_b128 v[224:227], v153 offset:52080
	ds_read_b128 v[228:231], v153 offset:52096
	ds_read_b128 v[232:235], v153 offset:62480
	ds_read_b128 v[236:239], v153 offset:62496
	ds_read_b128 v[240:243], v166
	ds_read_b128 v[244:247], v167
	ds_read_b128 v[248:251], v168
	ds_read_b128 v[252:255], v169
	s_waitcnt vmcnt(6) lgkmcnt(14)
	v_mfma_f32_32x32x16_f16 v[114:129], v[180:183], v[192:195], v[114:129]
	v_mfma_f32_32x32x16_f16 v[50:65], v[188:191], v[192:195], v[50:65]
	s_waitcnt lgkmcnt(13)
	v_mfma_f32_32x32x16_f16 v[98:113], v[180:183], v[200:203], v[98:113]
	v_mfma_f32_32x32x16_f16 v[34:49], v[188:191], v[200:203], v[34:49]
	s_waitcnt lgkmcnt(11)
	v_mfma_f32_32x32x16_f16 v[82:97], v[180:183], v[208:211], v[82:97]
	v_mfma_f32_32x32x16_f16 v[18:33], v[188:191], v[208:211], v[18:33]
	s_waitcnt lgkmcnt(9)
	v_mfma_f32_32x32x16_f16 v[66:81], v[180:183], v[216:219], v[66:81]
	v_mfma_f32_32x32x16_f16 v[2:17], v[188:191], v[216:219], v[2:17]
	s_add_i32 s6, s8, 0xffff8000
	v_lshl_add_u64 v[188:189], v[148:149], 0, s[6:7]
	global_load_dwordx4 v[180:183], v[188:189], off offset:16
	s_nop 0
	global_load_dwordx4 v[188:191], v[188:189], off offset:2064
	s_waitcnt vmcnt(6)
	v_mfma_f32_32x32x16_f16 v[114:129], v[176:179], v[196:199], v[114:129]
	v_mfma_f32_32x32x16_f16 v[50:65], v[184:187], v[196:199], v[50:65]
	v_mfma_f32_32x32x16_f16 v[98:113], v[176:179], v[204:207], v[98:113]
	v_mfma_f32_32x32x16_f16 v[34:49], v[184:187], v[204:207], v[34:49]
	v_mfma_f32_32x32x16_f16 v[82:97], v[176:179], v[212:215], v[82:97]
	v_mfma_f32_32x32x16_f16 v[18:33], v[184:187], v[212:215], v[18:33]
	s_waitcnt lgkmcnt(8)
	v_mfma_f32_32x32x16_f16 v[66:81], v[176:179], v[220:223], v[66:81]
	v_mfma_f32_32x32x16_f16 v[2:17], v[184:187], v[220:223], v[2:17]
	v_mfma_f32_32x32x16_f16 v[114:129], v[176:179], v[192:195], v[114:129]
	v_mfma_f32_32x32x16_f16 v[50:65], v[184:187], v[192:195], v[50:65]
	v_mfma_f32_32x32x16_f16 v[98:113], v[176:179], v[200:203], v[98:113]
	v_mfma_f32_32x32x16_f16 v[34:49], v[184:187], v[200:203], v[34:49]
	v_mfma_f32_32x32x16_f16 v[82:97], v[176:179], v[208:211], v[82:97]
	v_mfma_f32_32x32x16_f16 v[18:33], v[184:187], v[208:211], v[18:33]
	v_mfma_f32_32x32x16_f16 v[66:81], v[176:179], v[216:219], v[66:81]
	v_mfma_f32_32x32x16_f16 v[2:17], v[184:187], v[216:219], v[2:17]
	s_add_i32 s6, s8, 0xffff8000
	v_lshl_add_u64 v[184:185], v[148:149], 0, s[6:7]
	global_load_dwordx4 v[176:179], v[184:185], off
	s_nop 0
	global_load_dwordx4 v[184:187], v[184:185], off offset:2048
	ds_read_b128 v[192:195], v153 offset:57200
	ds_read_b128 v[196:199], v153 offset:57216
	ds_read_b128 v[200:203], v154
	ds_read_b128 v[204:207], v155
	ds_read_b128 v[208:211], v156
	ds_read_b128 v[212:215], v157
	ds_read_b128 v[216:219], v170
	ds_read_b128 v[220:223], v171
	s_waitcnt vmcnt(6) lgkmcnt(14)
	v_mfma_f32_32x32x16_f16 v[114:129], v[134:137], v[224:227], v[114:129]
	v_mfma_f32_32x32x16_f16 v[50:65], v[142:145], v[224:227], v[50:65]
	s_waitcnt lgkmcnt(13)
	v_mfma_f32_32x32x16_f16 v[98:113], v[134:137], v[232:235], v[98:113]
	v_mfma_f32_32x32x16_f16 v[34:49], v[142:145], v[232:235], v[34:49]
	s_waitcnt lgkmcnt(11)
	v_mfma_f32_32x32x16_f16 v[82:97], v[134:137], v[240:243], v[82:97]
	v_mfma_f32_32x32x16_f16 v[18:33], v[142:145], v[240:243], v[18:33]
	s_waitcnt lgkmcnt(9)
	v_mfma_f32_32x32x16_f16 v[66:81], v[134:137], v[248:251], v[66:81]
	v_mfma_f32_32x32x16_f16 v[2:17], v[142:145], v[248:251], v[2:17]
	s_add_i32 s6, s8, 0xffffc000
	v_lshl_add_u64 v[142:143], v[148:149], 0, s[6:7]
	global_load_dwordx4 v[134:137], v[142:143], off offset:16
	s_nop 0
	global_load_dwordx4 v[142:145], v[142:143], off offset:2064
	s_waitcnt vmcnt(6)
	v_mfma_f32_32x32x16_f16 v[114:129], v[130:133], v[228:231], v[114:129]
	v_mfma_f32_32x32x16_f16 v[50:65], v[138:141], v[228:231], v[50:65]
	v_mfma_f32_32x32x16_f16 v[98:113], v[130:133], v[236:239], v[98:113]
	v_mfma_f32_32x32x16_f16 v[34:49], v[138:141], v[236:239], v[34:49]
	v_mfma_f32_32x32x16_f16 v[82:97], v[130:133], v[244:247], v[82:97]
	v_mfma_f32_32x32x16_f16 v[18:33], v[138:141], v[244:247], v[18:33]
	s_waitcnt lgkmcnt(8)
	v_mfma_f32_32x32x16_f16 v[66:81], v[130:133], v[252:255], v[66:81]
	v_mfma_f32_32x32x16_f16 v[2:17], v[138:141], v[252:255], v[2:17]
	v_mfma_f32_32x32x16_f16 v[114:129], v[130:133], v[224:227], v[114:129]
	v_mfma_f32_32x32x16_f16 v[50:65], v[138:141], v[224:227], v[50:65]
	v_mfma_f32_32x32x16_f16 v[98:113], v[130:133], v[232:235], v[98:113]
	v_mfma_f32_32x32x16_f16 v[34:49], v[138:141], v[232:235], v[34:49]
	v_mfma_f32_32x32x16_f16 v[82:97], v[130:133], v[240:243], v[82:97]
	v_mfma_f32_32x32x16_f16 v[18:33], v[138:141], v[240:243], v[18:33]
	v_mfma_f32_32x32x16_f16 v[66:81], v[130:133], v[248:251], v[66:81]
	v_mfma_f32_32x32x16_f16 v[2:17], v[138:141], v[248:251], v[2:17]
	s_add_i32 s6, s8, 0xffffc000
	v_lshl_add_u64 v[138:139], v[148:149], 0, s[6:7]
	global_load_dwordx4 v[130:133], v[138:139], off
	s_nop 0
	global_load_dwordx4 v[138:141], v[138:139], off offset:2048
	ds_read_b128 v[224:227], v153 offset:59840
	ds_read_b128 v[228:231], v153 offset:59856
	ds_read_b128 v[232:235], v158
	ds_read_b128 v[236:239], v159
	ds_read_b128 v[240:243], v160
	ds_read_b128 v[244:247], v161
	ds_read_b128 v[248:251], v172
	ds_read_b128 v[252:255], v173
	s_waitcnt vmcnt(6) lgkmcnt(14)
	v_mfma_f32_32x32x16_f16 v[114:129], v[180:183], v[192:195], v[114:129]
	v_mfma_f32_32x32x16_f16 v[50:65], v[188:191], v[192:195], v[50:65]
	s_waitcnt lgkmcnt(13)
	v_mfma_f32_32x32x16_f16 v[98:113], v[180:183], v[200:203], v[98:113]
	v_mfma_f32_32x32x16_f16 v[34:49], v[188:191], v[200:203], v[34:49]
	s_waitcnt lgkmcnt(11)
	v_mfma_f32_32x32x16_f16 v[82:97], v[180:183], v[208:211], v[82:97]
	v_mfma_f32_32x32x16_f16 v[18:33], v[188:191], v[208:211], v[18:33]
	s_waitcnt lgkmcnt(9)
	v_mfma_f32_32x32x16_f16 v[66:81], v[180:183], v[216:219], v[66:81]
	v_mfma_f32_32x32x16_f16 v[2:17], v[188:191], v[216:219], v[2:17]
	s_mov_b32 s6, s8
	v_lshl_add_u64 v[188:189], v[148:149], 0, s[6:7]
	global_load_dwordx4 v[180:183], v[188:189], off offset:16
	s_nop 0
	global_load_dwordx4 v[188:191], v[188:189], off offset:2064
	s_waitcnt vmcnt(6)
	v_mfma_f32_32x32x16_f16 v[114:129], v[176:179], v[196:199], v[114:129]
	v_mfma_f32_32x32x16_f16 v[50:65], v[184:187], v[196:199], v[50:65]
	v_mfma_f32_32x32x16_f16 v[98:113], v[176:179], v[204:207], v[98:113]
	v_mfma_f32_32x32x16_f16 v[34:49], v[184:187], v[204:207], v[34:49]
	v_mfma_f32_32x32x16_f16 v[82:97], v[176:179], v[212:215], v[82:97]
	v_mfma_f32_32x32x16_f16 v[18:33], v[184:187], v[212:215], v[18:33]
	s_waitcnt lgkmcnt(8)
	v_mfma_f32_32x32x16_f16 v[66:81], v[176:179], v[220:223], v[66:81]
	v_mfma_f32_32x32x16_f16 v[2:17], v[184:187], v[220:223], v[2:17]
	v_mfma_f32_32x32x16_f16 v[114:129], v[176:179], v[192:195], v[114:129]
	v_mfma_f32_32x32x16_f16 v[50:65], v[184:187], v[192:195], v[50:65]
	v_mfma_f32_32x32x16_f16 v[98:113], v[176:179], v[200:203], v[98:113]
	v_mfma_f32_32x32x16_f16 v[34:49], v[184:187], v[200:203], v[34:49]
	v_mfma_f32_32x32x16_f16 v[82:97], v[176:179], v[208:211], v[82:97]
	v_mfma_f32_32x32x16_f16 v[18:33], v[184:187], v[208:211], v[18:33]
	v_mfma_f32_32x32x16_f16 v[66:81], v[176:179], v[216:219], v[66:81]
	v_mfma_f32_32x32x16_f16 v[2:17], v[184:187], v[216:219], v[2:17]
	s_mov_b32 s6, s8
	v_lshl_add_u64 v[184:185], v[148:149], 0, s[6:7]
	global_load_dwordx4 v[176:179], v[184:185], off
	s_nop 0
	global_load_dwordx4 v[184:187], v[184:185], off offset:2048
	ds_read_b128 v[192:195], v153 offset:57280
	ds_read_b128 v[196:199], v153 offset:57296
	ds_read_b128 v[200:203], v162
	ds_read_b128 v[204:207], v163
	ds_read_b128 v[208:211], v164
	ds_read_b128 v[212:215], v165
	ds_read_b128 v[216:219], v174
	ds_read_b128 v[220:223], v175
	s_waitcnt vmcnt(6) lgkmcnt(14)
	v_mfma_f32_32x32x16_f16 v[114:129], v[134:137], v[224:227], v[114:129]
	v_mfma_f32_32x32x16_f16 v[50:65], v[142:145], v[224:227], v[50:65]
	s_waitcnt lgkmcnt(13)
	v_mfma_f32_32x32x16_f16 v[98:113], v[134:137], v[232:235], v[98:113]
	v_mfma_f32_32x32x16_f16 v[34:49], v[142:145], v[232:235], v[34:49]
	s_waitcnt lgkmcnt(11)
	v_mfma_f32_32x32x16_f16 v[82:97], v[134:137], v[240:243], v[82:97]
	v_mfma_f32_32x32x16_f16 v[18:33], v[142:145], v[240:243], v[18:33]
	s_waitcnt lgkmcnt(9)
	v_mfma_f32_32x32x16_f16 v[66:81], v[134:137], v[248:251], v[66:81]
	v_mfma_f32_32x32x16_f16 v[2:17], v[142:145], v[248:251], v[2:17]
	s_min_u32 s6, s14, 62
	s_lshl_b32 s6, s6, 14
	s_add_i32 s6, s6, s12
	v_lshl_add_u64 v[142:143], v[148:149], 0, s[6:7]
	global_load_dwordx4 v[134:137], v[142:143], off offset:16
	s_nop 0
	global_load_dwordx4 v[142:145], v[142:143], off offset:2064
	s_waitcnt vmcnt(6)
	v_mfma_f32_32x32x16_f16 v[114:129], v[130:133], v[228:231], v[114:129]
	v_mfma_f32_32x32x16_f16 v[50:65], v[138:141], v[228:231], v[50:65]
	v_mfma_f32_32x32x16_f16 v[98:113], v[130:133], v[236:239], v[98:113]
	v_mfma_f32_32x32x16_f16 v[34:49], v[138:141], v[236:239], v[34:49]
	v_mfma_f32_32x32x16_f16 v[82:97], v[130:133], v[244:247], v[82:97]
	v_mfma_f32_32x32x16_f16 v[18:33], v[138:141], v[244:247], v[18:33]
	s_waitcnt lgkmcnt(8)
	v_mfma_f32_32x32x16_f16 v[66:81], v[130:133], v[252:255], v[66:81]
	v_mfma_f32_32x32x16_f16 v[2:17], v[138:141], v[252:255], v[2:17]
	v_mfma_f32_32x32x16_f16 v[114:129], v[130:133], v[224:227], v[114:129]
	v_mfma_f32_32x32x16_f16 v[50:65], v[138:141], v[224:227], v[50:65]
	v_mfma_f32_32x32x16_f16 v[98:113], v[130:133], v[232:235], v[98:113]
	v_mfma_f32_32x32x16_f16 v[34:49], v[138:141], v[232:235], v[34:49]
	v_mfma_f32_32x32x16_f16 v[82:97], v[130:133], v[240:243], v[82:97]
	v_mfma_f32_32x32x16_f16 v[18:33], v[138:141], v[240:243], v[18:33]
	v_mfma_f32_32x32x16_f16 v[66:81], v[130:133], v[248:251], v[66:81]
	v_mfma_f32_32x32x16_f16 v[2:17], v[138:141], v[248:251], v[2:17]
	s_min_u32 s6, s14, 62
	s_lshl_b32 s6, s6, 14
	s_add_i32 s6, s6, s12
	v_lshl_add_u64 v[138:139], v[148:149], 0, s[6:7]
	global_load_dwordx4 v[130:133], v[138:139], off
	s_nop 0
	global_load_dwordx4 v[138:141], v[138:139], off offset:2048
	s_waitcnt vmcnt(6) lgkmcnt(7)
	v_mfma_f32_32x32x16_f16 v[114:129], v[180:183], v[192:195], v[114:129]
	v_mfma_f32_32x32x16_f16 v[50:65], v[188:191], v[192:195], v[50:65]
	s_waitcnt lgkmcnt(5)
	v_mfma_f32_32x32x16_f16 v[98:113], v[180:183], v[200:203], v[98:113]
	v_mfma_f32_32x32x16_f16 v[34:49], v[188:191], v[200:203], v[34:49]
	s_waitcnt lgkmcnt(3)
	v_mfma_f32_32x32x16_f16 v[82:97], v[180:183], v[208:211], v[82:97]
	v_mfma_f32_32x32x16_f16 v[18:33], v[188:191], v[208:211], v[18:33]
	s_waitcnt lgkmcnt(1)
	v_mfma_f32_32x32x16_f16 v[66:81], v[180:183], v[216:219], v[66:81]
	v_mfma_f32_32x32x16_f16 v[2:17], v[188:191], v[216:219], v[2:17]
	s_add_i32 s6, s14, 1
	s_min_u32 s6, s6, 62
	s_lshl_b32 s6, s6, 14
	s_add_i32 s6, s6, s12
	v_lshl_add_u64 v[188:189], v[148:149], 0, s[6:7]
	global_load_dwordx4 v[180:183], v[188:189], off offset:16
	s_nop 0
	global_load_dwordx4 v[188:191], v[188:189], off offset:2064
	s_waitcnt vmcnt(6)
	v_mfma_f32_32x32x16_f16 v[114:129], v[176:179], v[196:199], v[114:129]
	v_mfma_f32_32x32x16_f16 v[50:65], v[184:187], v[196:199], v[50:65]
	v_mfma_f32_32x32x16_f16 v[98:113], v[176:179], v[204:207], v[98:113]
	v_mfma_f32_32x32x16_f16 v[34:49], v[184:187], v[204:207], v[34:49]
	v_mfma_f32_32x32x16_f16 v[82:97], v[176:179], v[212:215], v[82:97]
	v_mfma_f32_32x32x16_f16 v[18:33], v[184:187], v[212:215], v[18:33]
	s_waitcnt lgkmcnt(0)
	v_mfma_f32_32x32x16_f16 v[66:81], v[176:179], v[220:223], v[66:81]
	v_mfma_f32_32x32x16_f16 v[2:17], v[184:187], v[220:223], v[2:17]
	v_mfma_f32_32x32x16_f16 v[114:129], v[176:179], v[192:195], v[114:129]
	v_mfma_f32_32x32x16_f16 v[50:65], v[184:187], v[192:195], v[50:65]
	v_mfma_f32_32x32x16_f16 v[98:113], v[176:179], v[200:203], v[98:113]
	v_mfma_f32_32x32x16_f16 v[34:49], v[184:187], v[200:203], v[34:49]
	v_mfma_f32_32x32x16_f16 v[82:97], v[176:179], v[208:211], v[82:97]
	v_mfma_f32_32x32x16_f16 v[18:33], v[184:187], v[208:211], v[18:33]
	v_mfma_f32_32x32x16_f16 v[66:81], v[176:179], v[216:219], v[66:81]
	v_mfma_f32_32x32x16_f16 v[2:17], v[184:187], v[216:219], v[2:17]
	s_add_i32 s13, s13, 2
	s_add_i32 s8, s8, 0x48000
	s_add_i32 s14, s14, 18
	s_cmp_gt_u32 s13, 5
	s_barrier
	s_cbranch_scc0 .LBB5_2
	s_waitcnt vmcnt(0)
	s_and_b32 s6, s33, 0xc0
	s_waitcnt vmcnt(3)
	v_lshlrev_b32_e32 v134, 2, v151
	s_waitcnt vmcnt(1)
	v_or_b32_e32 v130, s6, v134
	s_waitcnt vmcnt(0)
	v_lshlrev_b32_e32 v139, 2, v130
	global_load_dwordx4 v[140:143], v139, s[10:11]
	s_mul_i32 s7, s5, 0x8800
	v_lshlrev_b32_e32 v135, 3, v151
	s_movk_i32 s8, 0x110
	v_or_b32_e32 v130, s7, v135
	v_mad_u32_u24 v138, v150, s8, v130
	global_load_dwordx4 v[130:133], v139, s[10:11] offset:32
	s_mov_b32 s6, 0x41800000
	v_add_u32_e32 v137, 0x2000, v138
	v_add_u32_e32 v136, 0x4000, v138
	s_waitcnt vmcnt(1)
	v_fmamk_f32 v114, v114, 0x3a800000, v140
	v_fmamk_f32 v116, v116, 0x3a800000, v142
	v_fmamk_f32 v117, v117, 0x3a800000, v143
	v_fmamk_f32 v115, v115, 0x3a800000, v141
	v_fmamk_f32 v98, v98, 0x3a800000, v140
	v_fmamk_f32 v99, v99, 0x3a800000, v141
	v_fmamk_f32 v82, v82, 0x3a800000, v140
	v_fmamk_f32 v83, v83, 0x3a800000, v141
	v_fmamk_f32 v84, v84, 0x3a800000, v142
	v_fmamk_f32 v85, v85, 0x3a800000, v143
	v_fmamk_f32 v140, v66, 0x3a800000, v140
	v_fmamk_f32 v141, v67, 0x3a800000, v141
	v_max_f32_e32 v144, 0, v114
	v_max_f32_e32 v66, 0, v116
	v_max_f32_e32 v67, 0, v117
	v_fmamk_f32 v101, v101, 0x3a800000, v143
	v_fmac_f32_e32 v143, 0x3a800000, v69
	v_max_f32_e32 v153, 0, v115
	v_max_f32_e32 v145, 0, v98
	v_max_f32_e32 v156, 0, v99
	v_max_f32_e32 v148, 0, v82
	v_max_f32_e32 v160, 0, v83
	v_max_f32_e32 v82, 0, v84
	v_max_f32_e32 v83, 0, v85
	v_max_f32_e32 v154, 0, v140
	v_fma_mixlo_f16 v140, v144, s6, 0
	v_pk_mul_f32 v[98:99], v[66:67], s[6:7] op_sel_hi:[1,0]
	v_max_f32_e32 v85, 0, v143
	v_fma_mixlo_f16 v155, v153, s6, 0
	v_mul_f32_e32 v149, 0x41800000, v145
	v_mul_f32_e32 v158, 0x41800000, v156
	v_pk_mul_f32 v[114:115], v[82:83], s[6:7] op_sel_hi:[1,0]
	v_fma_mixlo_f16 v167, v154, s6, 0
	v_fma_mixlo_f16 v140, v144, s6, -v140 op_sel_hi:[0,0,1]
	v_cvt_pk_f16_f32 v143, v98, v99
	v_max_f32_e32 v161, 0, v141
	v_mul_f32_e32 v141, 0x41800000, v144
	v_mul_f32_e32 v166, 0x41800000, v154
	v_cvt_pk_f16_f32 v144, v149, v158
	v_cvt_pk_f16_f32 v149, v114, v115
	v_fma_mixlo_f16 v114, v154, s6, -v167 op_sel_hi:[0,0,1]
	v_fma_mixhi_f16 v140, v153, s6, -v155 op_sel_hi:[0,0,1]
	v_cvt_f32_f16_e32 v154, v143
	v_cvt_f32_f16_sdwa v155, v143 dst_sel:DWORD dst_unused:UNUSED_PAD src0_sel:WORD_1
	v_fmamk_f32 v100, v100, 0x3a800000, v142
	v_fmamk_f32 v142, v68, 0x3a800000, v142
	v_max_f32_e32 v84, 0, v142
	v_pk_mul_f32 v[116:117], v[84:85], s[6:7] op_sel_hi:[1,0]
	v_mul_f32_e32 v142, 0x41800000, v153
	v_cvt_pk_f16_f32 v117, v116, v117
	v_pk_fma_f32 v[66:67], v[66:67], s[6:7], v[154:155] op_sel_hi:[1,0,1] neg_lo:[0,0,1] neg_hi:[0,0,1]
	v_max_f32_e32 v68, 0, v100
	v_max_f32_e32 v69, 0, v101
	v_cvt_pk_f16_f32 v142, v141, v142
	v_cvt_pk_f16_f32 v141, v66, v67
	v_cvt_f32_f16_e32 v66, v117
	v_cvt_f32_f16_sdwa v67, v117 dst_sel:DWORD dst_unused:UNUSED_PAD src0_sel:WORD_1
	v_fma_mixlo_f16 v157, v145, s6, 0
	v_pk_mul_f32 v[100:101], v[68:69], s[6:7] op_sel_hi:[1,0]
	v_fma_mixlo_f16 v159, v156, s6, 0
	v_fma_mixlo_f16 v98, v145, s6, -v157 op_sel_hi:[0,0,1]
	v_cvt_pk_f16_f32 v145, v100, v101
	v_fma_mixhi_f16 v98, v156, s6, -v159 op_sel_hi:[0,0,1]
	v_cvt_f32_f16_e32 v156, v145
	v_cvt_f32_f16_sdwa v157, v145 dst_sel:DWORD dst_unused:UNUSED_PAD src0_sel:WORD_1
	v_cvt_f32_f16_e32 v158, v149
	v_cvt_f32_f16_sdwa v159, v149 dst_sel:DWORD dst_unused:UNUSED_PAD src0_sel:WORD_1
	v_pk_fma_f32 v[66:67], v[84:85], s[6:7], v[66:67] op_sel_hi:[1,0,1] neg_lo:[0,0,1] neg_hi:[0,0,1]
	v_fma_mixlo_f16 v163, v148, s6, 0
	v_cvt_pk_f16_f32 v115, v66, v67
	s_waitcnt vmcnt(0)
	v_fmamk_f32 v66, v118, 0x3a800000, v130
	v_max_f32_e32 v66, 0, v66
	v_pk_fma_f32 v[68:69], v[68:69], s[6:7], v[156:157] op_sel_hi:[1,0,1] neg_lo:[0,0,1] neg_hi:[0,0,1]
	v_pk_fma_f32 v[82:83], v[82:83], s[6:7], v[158:159] op_sel_hi:[1,0,1] neg_lo:[0,0,1] neg_hi:[0,0,1]
	v_fma_mixlo_f16 v67, v66, s6, 0
	v_mul_f32_e32 v162, 0x41800000, v148
	v_mul_f32_e32 v164, 0x41800000, v160
	v_fma_mixlo_f16 v165, v160, s6, 0
	v_fma_mixlo_f16 v100, v148, s6, -v163 op_sel_hi:[0,0,1]
	v_cvt_pk_f16_f32 v99, v68, v69
	v_cvt_pk_f16_f32 v101, v82, v83
	v_mul_f32_e32 v83, 0x41800000, v66
	v_fma_mixlo_f16 v84, v66, s6, -v67 op_sel_hi:[0,0,1]
	v_fmamk_f32 v66, v119, 0x3a800000, v131
	v_cvt_pk_f16_f32 v148, v162, v164
	v_fma_mixhi_f16 v100, v160, s6, -v165 op_sel_hi:[0,0,1]
	ds_write2_b64 v138, v[142:143], v[140:141] offset1:2
	ds_write2_b64 v137, v[144:145], v[98:99] offset0:64 offset1:66
	ds_write2_b64 v136, v[148:149], v[100:101] offset0:128 offset1:130
	v_max_f32_e32 v85, 0, v66
	v_fmamk_f32 v66, v120, 0x3a800000, v132
	v_fmamk_f32 v99, v121, 0x3a800000, v133
	v_max_f32_e32 v98, 0, v66
	v_max_f32_e32 v99, 0, v99
	v_mul_f32_e32 v168, 0x41800000, v161
	v_fma_mixlo_f16 v68, v161, s6, 0
	v_pk_mul_f32 v[100:101], v[98:99], s[6:7] op_sel_hi:[1,0]
	v_cvt_pk_f16_f32 v116, v166, v168
	v_fma_mixhi_f16 v114, v161, s6, -v68 op_sel_hi:[0,0,1]
	v_add_u32_e32 v82, 0x6000, v138
	v_cvt_pk_f16_f32 v101, v100, v101
	ds_write2_b64 v82, v[116:117], v[114:115] offset0:192 offset1:194
	v_cvt_f32_f16_e32 v114, v101
	v_cvt_f32_f16_sdwa v115, v101 dst_sel:DWORD dst_unused:UNUSED_PAD src0_sel:WORD_1
	global_load_dwordx4 v[66:69], v139, s[10:11] offset:64
	v_fma_mixlo_f16 v117, v85, s6, 0
	v_mul_f32_e32 v116, 0x41800000, v85
	v_pk_fma_f32 v[98:99], v[98:99], s[6:7], v[114:115] op_sel_hi:[1,0,1] neg_lo:[0,0,1] neg_hi:[0,0,1]
	v_fma_mixhi_f16 v84, v85, s6, -v117 op_sel_hi:[0,0,1]
	v_cvt_pk_f16_f32 v85, v98, v99
	v_fmamk_f32 v98, v104, 0x3a800000, v132
	v_fmamk_f32 v99, v105, 0x3a800000, v133
	v_cvt_pk_f16_f32 v100, v83, v116
	v_fmamk_f32 v83, v102, 0x3a800000, v130
	v_max_f32_e32 v98, 0, v98
	v_max_f32_e32 v99, 0, v99
	ds_write2_b64 v138, v[100:101], v[84:85] offset0:4 offset1:6
	v_max_f32_e32 v83, 0, v83
	v_pk_mul_f32 v[100:101], v[98:99], s[6:7] op_sel_hi:[1,0]
	v_fma_mixlo_f16 v84, v83, s6, 0
	v_cvt_pk_f16_f32 v101, v100, v101
	v_mul_f32_e32 v85, 0x41800000, v83
	v_fma_mixlo_f16 v84, v83, s6, -v84 op_sel_hi:[0,0,1]
	v_fmamk_f32 v83, v103, 0x3a800000, v131
	v_cvt_f32_f16_e32 v102, v101
	v_cvt_f32_f16_sdwa v103, v101 dst_sel:DWORD dst_unused:UNUSED_PAD src0_sel:WORD_1
	v_max_f32_e32 v83, 0, v83
	v_fma_mixlo_f16 v104, v83, s6, 0
	v_mul_f32_e32 v114, 0x41800000, v83
	v_fma_mixhi_f16 v84, v83, s6, -v104 op_sel_hi:[0,0,1]
	v_pk_fma_f32 v[98:99], v[98:99], s[6:7], v[102:103] op_sel_hi:[1,0,1] neg_lo:[0,0,1] neg_hi:[0,0,1]
	v_fmamk_f32 v83, v86, 0x3a800000, v130
	v_cvt_pk_f16_f32 v100, v85, v114
	v_cvt_pk_f16_f32 v85, v98, v99
	v_max_f32_e32 v83, 0, v83
	ds_write2_b64 v137, v[100:101], v[84:85] offset0:68 offset1:70
	v_fma_mixlo_f16 v84, v83, s6, 0
	v_mul_f32_e32 v85, 0x41800000, v83
	v_fma_mixlo_f16 v84, v83, s6, -v84 op_sel_hi:[0,0,1]
	v_fmamk_f32 v83, v87, 0x3a800000, v131
	v_fmamk_f32 v86, v88, 0x3a800000, v132
	v_fmamk_f32 v87, v89, 0x3a800000, v133
	v_max_f32_e32 v86, 0, v86
	v_max_f32_e32 v87, 0, v87
	v_pk_mul_f32 v[88:89], v[86:87], s[6:7] op_sel_hi:[1,0]
	v_max_f32_e32 v83, 0, v83
	v_cvt_pk_f16_f32 v89, v88, v89
	v_cvt_f32_f16_e32 v98, v89
	v_cvt_f32_f16_sdwa v99, v89 dst_sel:DWORD dst_unused:UNUSED_PAD src0_sel:WORD_1
	v_mul_f32_e32 v100, 0x41800000, v83
	v_fma_mixlo_f16 v101, v83, s6, 0
	v_fmamk_f32 v70, v70, 0x3a800000, v130
	v_pk_fma_f32 v[86:87], v[86:87], s[6:7], v[98:99] op_sel_hi:[1,0,1] neg_lo:[0,0,1] neg_hi:[0,0,1]
	v_cvt_pk_f16_f32 v88, v85, v100
	v_fma_mixhi_f16 v84, v83, s6, -v101 op_sel_hi:[0,0,1]
	v_cvt_pk_f16_f32 v85, v86, v87
	v_max_f32_e32 v70, 0, v70
	v_fmamk_f32 v72, v72, 0x3a800000, v132
	v_fmac_f32_e32 v133, 0x3a800000, v73
	ds_write2_b64 v136, v[88:89], v[84:85] offset0:132 offset1:134
	v_fma_mixlo_f16 v84, v70, s6, 0
	v_max_f32_e32 v72, 0, v72
	v_max_f32_e32 v73, 0, v133
	v_mul_f32_e32 v83, 0x41800000, v70
	v_fma_mixlo_f16 v70, v70, s6, -v84 op_sel_hi:[0,0,1]
	v_pk_mul_f32 v[84:85], v[72:73], s[6:7] op_sel_hi:[1,0]
	v_fmamk_f32 v71, v71, 0x3a800000, v131
	v_cvt_pk_f16_f32 v85, v84, v85
	v_cvt_f32_f16_e32 v86, v85
	v_cvt_f32_f16_sdwa v87, v85 dst_sel:DWORD dst_unused:UNUSED_PAD src0_sel:WORD_1
	v_max_f32_e32 v71, 0, v71
	v_mul_f32_e32 v88, 0x41800000, v71
	v_fma_mixlo_f16 v89, v71, s6, 0
	v_pk_fma_f32 v[72:73], v[72:73], s[6:7], v[86:87] op_sel_hi:[1,0,1] neg_lo:[0,0,1] neg_hi:[0,0,1]
	v_cvt_pk_f16_f32 v84, v83, v88
	v_fma_mixhi_f16 v70, v71, s6, -v89 op_sel_hi:[0,0,1]
	v_cvt_pk_f16_f32 v71, v72, v73
	ds_write2_b64 v82, v[84:85], v[70:71] offset0:196 offset1:198
	global_load_dwordx4 v[70:73], v139, s[10:11] offset:96
	s_waitcnt vmcnt(1)
	v_fmamk_f32 v86, v124, 0x3a800000, v68
	v_fmamk_f32 v87, v125, 0x3a800000, v69
	v_max_f32_e32 v86, 0, v86
	v_max_f32_e32 v87, 0, v87
	v_pk_mul_f32 v[88:89], v[86:87], s[6:7] op_sel_hi:[1,0]
	v_fmamk_f32 v83, v122, 0x3a800000, v66
	v_cvt_pk_f16_f32 v89, v88, v89
	v_max_f32_e32 v83, 0, v83
	v_cvt_f32_f16_e32 v98, v89
	v_cvt_f32_f16_sdwa v99, v89 dst_sel:DWORD dst_unused:UNUSED_PAD src0_sel:WORD_1
	v_fma_mixlo_f16 v84, v83, s6, 0
	v_mul_f32_e32 v85, 0x41800000, v83
	v_fma_mixlo_f16 v84, v83, s6, -v84 op_sel_hi:[0,0,1]
	v_fmamk_f32 v83, v123, 0x3a800000, v67
	v_max_f32_e32 v83, 0, v83
	v_mul_f32_e32 v100, 0x41800000, v83
	v_pk_fma_f32 v[86:87], v[86:87], s[6:7], v[98:99] op_sel_hi:[1,0,1] neg_lo:[0,0,1] neg_hi:[0,0,1]
	v_fma_mixlo_f16 v101, v83, s6, 0
	v_cvt_pk_f16_f32 v88, v85, v100
	v_cvt_pk_f16_f32 v85, v86, v87
	v_fmamk_f32 v86, v108, 0x3a800000, v68
	v_fmamk_f32 v87, v109, 0x3a800000, v69
	v_fma_mixhi_f16 v84, v83, s6, -v101 op_sel_hi:[0,0,1]
	v_max_f32_e32 v86, 0, v86
	v_max_f32_e32 v87, 0, v87
	ds_write2_b64 v138, v[88:89], v[84:85] offset0:8 offset1:10
	v_fmamk_f32 v83, v106, 0x3a800000, v66
	v_pk_mul_f32 v[88:89], v[86:87], s[6:7] op_sel_hi:[1,0]
	v_max_f32_e32 v83, 0, v83
	v_cvt_pk_f16_f32 v89, v88, v89
	v_fma_mixlo_f16 v84, v83, s6, 0
	v_cvt_f32_f16_e32 v98, v89
	v_cvt_f32_f16_sdwa v99, v89 dst_sel:DWORD dst_unused:UNUSED_PAD src0_sel:WORD_1
	v_mul_f32_e32 v85, 0x41800000, v83
	v_fma_mixlo_f16 v84, v83, s6, -v84 op_sel_hi:[0,0,1]
	v_fmamk_f32 v83, v107, 0x3a800000, v67
	v_max_f32_e32 v83, 0, v83
	v_fma_mixlo_f16 v101, v83, s6, 0
	v_mul_f32_e32 v100, 0x41800000, v83
	v_fma_mixhi_f16 v84, v83, s6, -v101 op_sel_hi:[0,0,1]
	v_pk_fma_f32 v[86:87], v[86:87], s[6:7], v[98:99] op_sel_hi:[1,0,1] neg_lo:[0,0,1] neg_hi:[0,0,1]
	v_fmamk_f32 v83, v90, 0x3a800000, v66
	v_cvt_pk_f16_f32 v88, v85, v100
	v_cvt_pk_f16_f32 v85, v86, v87
	v_max_f32_e32 v83, 0, v83
	ds_write2_b64 v137, v[88:89], v[84:85] offset0:72 offset1:74
	v_fma_mixlo_f16 v84, v83, s6, 0
	v_fmamk_f32 v86, v92, 0x3a800000, v68
	v_fmamk_f32 v87, v93, 0x3a800000, v69
	v_mul_f32_e32 v85, 0x41800000, v83
	v_fma_mixlo_f16 v84, v83, s6, -v84 op_sel_hi:[0,0,1]
	v_fmamk_f32 v83, v91, 0x3a800000, v67
	v_max_f32_e32 v86, 0, v86
	v_max_f32_e32 v87, 0, v87
	v_fmamk_f32 v66, v74, 0x3a800000, v66
	v_max_f32_e32 v83, 0, v83
	v_pk_mul_f32 v[88:89], v[86:87], s[6:7] op_sel_hi:[1,0]
	v_max_f32_e32 v66, 0, v66
	v_fmamk_f32 v68, v76, 0x3a800000, v68
	v_fmac_f32_e32 v69, 0x3a800000, v77
	v_cvt_pk_f16_f32 v89, v88, v89
	v_fma_mixlo_f16 v92, v83, s6, 0
	v_fma_mixlo_f16 v74, v66, s6, 0
	v_max_f32_e32 v68, 0, v68
	v_max_f32_e32 v69, 0, v69
	v_mul_f32_e32 v98, 0x41800000, v83
	v_cvt_f32_f16_e32 v90, v89
	v_cvt_f32_f16_sdwa v91, v89 dst_sel:DWORD dst_unused:UNUSED_PAD src0_sel:WORD_1
	v_fma_mixhi_f16 v84, v83, s6, -v92 op_sel_hi:[0,0,1]
	v_mul_f32_e32 v83, 0x41800000, v66
	v_fma_mixlo_f16 v66, v66, s6, -v74 op_sel_hi:[0,0,1]
	v_fmamk_f32 v67, v75, 0x3a800000, v67
	v_pk_mul_f32 v[74:75], v[68:69], s[6:7] op_sel_hi:[1,0]
	v_pk_fma_f32 v[86:87], v[86:87], s[6:7], v[90:91] op_sel_hi:[1,0,1] neg_lo:[0,0,1] neg_hi:[0,0,1]
	v_cvt_pk_f16_f32 v75, v74, v75
	v_cvt_f32_f16_e32 v76, v75
	v_cvt_f32_f16_sdwa v77, v75 dst_sel:DWORD dst_unused:UNUSED_PAD src0_sel:WORD_1
	v_cvt_pk_f16_f32 v88, v85, v98
	v_cvt_pk_f16_f32 v85, v86, v87
	v_max_f32_e32 v67, 0, v67
	ds_write2_b64 v136, v[88:89], v[84:85] offset0:136 offset1:138
	v_mul_f32_e32 v84, 0x41800000, v67
	v_fma_mixlo_f16 v85, v67, s6, 0
	v_pk_fma_f32 v[68:69], v[68:69], s[6:7], v[76:77] op_sel_hi:[1,0,1] neg_lo:[0,0,1] neg_hi:[0,0,1]
	v_cvt_pk_f16_f32 v74, v83, v84
	v_fma_mixhi_f16 v66, v67, s6, -v85 op_sel_hi:[0,0,1]
	v_cvt_pk_f16_f32 v67, v68, v69
	ds_write2_b64 v82, v[74:75], v[66:67] offset0:200 offset1:202
	s_waitcnt vmcnt(0)
	v_fmamk_f32 v66, v126, 0x3a800000, v70
	v_max_f32_e32 v66, 0, v66
	v_fma_mixlo_f16 v67, v66, s6, 0
	v_mul_f32_e32 v75, 0x41800000, v66
	v_fma_mixlo_f16 v74, v66, s6, -v67 op_sel_hi:[0,0,1]
	v_fmamk_f32 v66, v127, 0x3a800000, v71
	v_max_f32_e32 v83, 0, v66
	v_fmamk_f32 v66, v128, 0x3a800000, v72
	v_fmamk_f32 v77, v129, 0x3a800000, v73
	v_max_f32_e32 v76, 0, v66
	v_max_f32_e32 v77, 0, v77
	v_pk_mul_f32 v[84:85], v[76:77], s[6:7] op_sel_hi:[1,0]
	v_mul_f32_e32 v88, 0x41800000, v83
	v_cvt_pk_f16_f32 v85, v84, v85
	v_cvt_f32_f16_e32 v86, v85
	v_cvt_f32_f16_sdwa v87, v85 dst_sel:DWORD dst_unused:UNUSED_PAD src0_sel:WORD_1
	v_fma_mixlo_f16 v89, v83, s6, 0
	global_load_dwordx4 v[66:69], v139, s[10:11] offset:128
	v_cvt_pk_f16_f32 v84, v75, v88
	v_pk_fma_f32 v[76:77], v[76:77], s[6:7], v[86:87] op_sel_hi:[1,0,1] neg_lo:[0,0,1] neg_hi:[0,0,1]
	v_fma_mixhi_f16 v74, v83, s6, -v89 op_sel_hi:[0,0,1]
	v_cvt_pk_f16_f32 v75, v76, v77
	ds_write2_b64 v138, v[84:85], v[74:75] offset0:12 offset1:14
	v_fmamk_f32 v74, v110, 0x3a800000, v70
	v_max_f32_e32 v74, 0, v74
	v_fma_mixlo_f16 v76, v74, s6, 0
	v_mul_f32_e32 v75, 0x41800000, v74
	v_fma_mixlo_f16 v74, v74, s6, -v76 op_sel_hi:[0,0,1]
	v_fmamk_f32 v76, v111, 0x3a800000, v71
	v_max_f32_e32 v83, 0, v76
	v_fmamk_f32 v76, v112, 0x3a800000, v72
	v_fmamk_f32 v77, v113, 0x3a800000, v73
	v_max_f32_e32 v76, 0, v76
	v_max_f32_e32 v77, 0, v77
	v_pk_mul_f32 v[84:85], v[76:77], s[6:7] op_sel_hi:[1,0]
	v_mul_f32_e32 v88, 0x41800000, v83
	v_cvt_pk_f16_f32 v85, v84, v85
	v_cvt_f32_f16_e32 v86, v85
	v_cvt_f32_f16_sdwa v87, v85 dst_sel:DWORD dst_unused:UNUSED_PAD src0_sel:WORD_1
	v_fma_mixlo_f16 v89, v83, s6, 0
	v_cvt_pk_f16_f32 v84, v75, v88
	v_fma_mixhi_f16 v74, v83, s6, -v89 op_sel_hi:[0,0,1]
	v_pk_fma_f32 v[76:77], v[76:77], s[6:7], v[86:87] op_sel_hi:[1,0,1] neg_lo:[0,0,1] neg_hi:[0,0,1]
	s_nop 0
	v_cvt_pk_f16_f32 v75, v76, v77
	ds_write2_b64 v137, v[84:85], v[74:75] offset0:76 offset1:78
	v_fmamk_f32 v74, v94, 0x3a800000, v70
	v_max_f32_e32 v74, 0, v74
	v_fma_mixlo_f16 v76, v74, s6, 0
	v_mul_f32_e32 v75, 0x41800000, v74
	v_fma_mixlo_f16 v74, v74, s6, -v76 op_sel_hi:[0,0,1]
	v_fmamk_f32 v76, v95, 0x3a800000, v71
	v_max_f32_e32 v83, 0, v76
	v_fmamk_f32 v76, v96, 0x3a800000, v72
	v_fmamk_f32 v77, v97, 0x3a800000, v73
	v_max_f32_e32 v76, 0, v76
	v_max_f32_e32 v77, 0, v77
	v_pk_mul_f32 v[84:85], v[76:77], s[6:7] op_sel_hi:[1,0]
	v_mul_f32_e32 v88, 0x41800000, v83
	v_cvt_pk_f16_f32 v85, v84, v85
	v_cvt_f32_f16_e32 v86, v85
	v_cvt_f32_f16_sdwa v87, v85 dst_sel:DWORD dst_unused:UNUSED_PAD src0_sel:WORD_1
	v_fma_mixlo_f16 v89, v83, s6, 0
	v_fmamk_f32 v70, v78, 0x3a800000, v70
	v_cvt_pk_f16_f32 v84, v75, v88
	v_pk_fma_f32 v[76:77], v[76:77], s[6:7], v[86:87] op_sel_hi:[1,0,1] neg_lo:[0,0,1] neg_hi:[0,0,1]
	v_fma_mixhi_f16 v74, v83, s6, -v89 op_sel_hi:[0,0,1]
	v_cvt_pk_f16_f32 v75, v76, v77
	v_max_f32_e32 v70, 0, v70
	v_fmamk_f32 v72, v80, 0x3a800000, v72
	v_fmac_f32_e32 v73, 0x3a800000, v81
	ds_write2_b64 v136, v[84:85], v[74:75] offset0:140 offset1:142
	v_fma_mixlo_f16 v74, v70, s6, 0
	v_max_f32_e32 v72, 0, v72
	v_max_f32_e32 v73, 0, v73
	v_mul_f32_e32 v78, 0x41800000, v70
	v_fma_mixlo_f16 v70, v70, s6, -v74 op_sel_hi:[0,0,1]
	v_pk_mul_f32 v[74:75], v[72:73], s[6:7] op_sel_hi:[1,0]
	v_fmamk_f32 v71, v79, 0x3a800000, v71
	v_cvt_pk_f16_f32 v75, v74, v75
	v_cvt_f32_f16_e32 v76, v75
	v_cvt_f32_f16_sdwa v77, v75 dst_sel:DWORD dst_unused:UNUSED_PAD src0_sel:WORD_1
	v_max_f32_e32 v71, 0, v71
	v_mul_f32_e32 v79, 0x41800000, v71
	v_fma_mixlo_f16 v80, v71, s6, 0
	v_pk_fma_f32 v[72:73], v[72:73], s[6:7], v[76:77] op_sel_hi:[1,0,1] neg_lo:[0,0,1] neg_hi:[0,0,1]
	v_cvt_pk_f16_f32 v74, v78, v79
	v_fma_mixhi_f16 v70, v71, s6, -v80 op_sel_hi:[0,0,1]
	v_cvt_pk_f16_f32 v71, v72, v73
	ds_write2_b64 v82, v[74:75], v[70:71] offset0:204 offset1:206
	global_load_dwordx4 v[70:73], v139, s[10:11] offset:160
	s_waitcnt vmcnt(1)
	v_fmamk_f32 v50, v50, 0x3a800000, v66
	v_max_f32_e32 v50, 0, v50
	v_fmamk_f32 v52, v52, 0x3a800000, v68
	v_fmamk_f32 v53, v53, 0x3a800000, v69
	v_fma_mixlo_f16 v74, v50, s6, 0
	v_max_f32_e32 v52, 0, v52
	v_max_f32_e32 v53, 0, v53
	v_mul_f32_e32 v78, 0x41800000, v50
	v_fma_mixlo_f16 v50, v50, s6, -v74 op_sel_hi:[0,0,1]
	v_pk_mul_f32 v[74:75], v[52:53], s[6:7] op_sel_hi:[1,0]
	v_fmamk_f32 v51, v51, 0x3a800000, v67
	v_cvt_pk_f16_f32 v75, v74, v75
	v_cvt_f32_f16_e32 v76, v75
	v_cvt_f32_f16_sdwa v77, v75 dst_sel:DWORD dst_unused:UNUSED_PAD src0_sel:WORD_1
	v_max_f32_e32 v51, 0, v51
	v_mul_f32_e32 v79, 0x41800000, v51
	v_fma_mixlo_f16 v80, v51, s6, 0
	v_pk_fma_f32 v[52:53], v[52:53], s[6:7], v[76:77] op_sel_hi:[1,0,1] neg_lo:[0,0,1] neg_hi:[0,0,1]
	v_fmamk_f32 v34, v34, 0x3a800000, v66
	v_cvt_pk_f16_f32 v74, v78, v79
	v_fma_mixhi_f16 v50, v51, s6, -v80 op_sel_hi:[0,0,1]
	v_cvt_pk_f16_f32 v51, v52, v53
	v_max_f32_e32 v34, 0, v34
	v_fmamk_f32 v36, v36, 0x3a800000, v68
	v_fmamk_f32 v37, v37, 0x3a800000, v69
	ds_write2_b64 v138, v[74:75], v[50:51] offset0:16 offset1:18
	v_fma_mixlo_f16 v50, v34, s6, 0
	v_max_f32_e32 v36, 0, v36
	v_max_f32_e32 v37, 0, v37
	v_mul_f32_e32 v74, 0x41800000, v34
	v_fma_mixlo_f16 v34, v34, s6, -v50 op_sel_hi:[0,0,1]
	v_pk_mul_f32 v[50:51], v[36:37], s[6:7] op_sel_hi:[1,0]
	v_fmamk_f32 v35, v35, 0x3a800000, v67
	v_cvt_pk_f16_f32 v51, v50, v51
	v_cvt_f32_f16_e32 v52, v51
	v_cvt_f32_f16_sdwa v53, v51 dst_sel:DWORD dst_unused:UNUSED_PAD src0_sel:WORD_1
	v_max_f32_e32 v35, 0, v35
	v_mul_f32_e32 v75, 0x41800000, v35
	v_fma_mixlo_f16 v76, v35, s6, 0
	v_pk_fma_f32 v[36:37], v[36:37], s[6:7], v[52:53] op_sel_hi:[1,0,1] neg_lo:[0,0,1] neg_hi:[0,0,1]
	v_fmamk_f32 v18, v18, 0x3a800000, v66
	v_cvt_pk_f16_f32 v50, v74, v75
	v_fma_mixhi_f16 v34, v35, s6, -v76 op_sel_hi:[0,0,1]
	v_cvt_pk_f16_f32 v35, v36, v37
	v_max_f32_e32 v18, 0, v18
	v_fmamk_f32 v20, v20, 0x3a800000, v68
	v_fmamk_f32 v21, v21, 0x3a800000, v69
	ds_write2_b64 v137, v[50:51], v[34:35] offset0:80 offset1:82
	v_fma_mixlo_f16 v34, v18, s6, 0
	v_max_f32_e32 v20, 0, v20
	v_max_f32_e32 v21, 0, v21
	v_mul_f32_e32 v50, 0x41800000, v18
	v_fma_mixlo_f16 v18, v18, s6, -v34 op_sel_hi:[0,0,1]
	v_pk_mul_f32 v[34:35], v[20:21], s[6:7] op_sel_hi:[1,0]
	v_fmamk_f32 v19, v19, 0x3a800000, v67
	v_cvt_pk_f16_f32 v35, v34, v35
	v_cvt_f32_f16_e32 v36, v35
	v_cvt_f32_f16_sdwa v37, v35 dst_sel:DWORD dst_unused:UNUSED_PAD src0_sel:WORD_1
	v_max_f32_e32 v19, 0, v19
	v_mul_f32_e32 v51, 0x41800000, v19
	v_fma_mixlo_f16 v52, v19, s6, 0
	v_pk_fma_f32 v[20:21], v[20:21], s[6:7], v[36:37] op_sel_hi:[1,0,1] neg_lo:[0,0,1] neg_hi:[0,0,1]
	v_fmamk_f32 v2, v2, 0x3a800000, v66
	v_cvt_pk_f16_f32 v34, v50, v51
	v_fma_mixhi_f16 v18, v19, s6, -v52 op_sel_hi:[0,0,1]
	v_cvt_pk_f16_f32 v19, v20, v21
	v_max_f32_e32 v2, 0, v2
	v_fmamk_f32 v4, v4, 0x3a800000, v68
	v_fmac_f32_e32 v69, 0x3a800000, v5
	ds_write2_b64 v136, v[34:35], v[18:19] offset0:144 offset1:146
	v_fma_mixlo_f16 v18, v2, s6, 0
	v_max_f32_e32 v4, 0, v4
	v_max_f32_e32 v5, 0, v69
	v_mul_f32_e32 v34, 0x41800000, v2
	v_fma_mixlo_f16 v2, v2, s6, -v18 op_sel_hi:[0,0,1]
	v_pk_mul_f32 v[18:19], v[4:5], s[6:7] op_sel_hi:[1,0]
	v_fmamk_f32 v3, v3, 0x3a800000, v67
	v_cvt_pk_f16_f32 v19, v18, v19
	v_cvt_f32_f16_e32 v20, v19
	v_cvt_f32_f16_sdwa v21, v19 dst_sel:DWORD dst_unused:UNUSED_PAD src0_sel:WORD_1
	v_max_f32_e32 v3, 0, v3
	v_mul_f32_e32 v35, 0x41800000, v3
	v_fma_mixlo_f16 v36, v3, s6, 0
	v_pk_fma_f32 v[4:5], v[4:5], s[6:7], v[20:21] op_sel_hi:[1,0,1] neg_lo:[0,0,1] neg_hi:[0,0,1]
	v_cvt_pk_f16_f32 v18, v34, v35
	v_fma_mixhi_f16 v2, v3, s6, -v36 op_sel_hi:[0,0,1]
	v_cvt_pk_f16_f32 v3, v4, v5
	ds_write2_b64 v82, v[18:19], v[2:3] offset0:208 offset1:210
	s_waitcnt vmcnt(0)
	v_fmamk_f32 v2, v54, 0x3a800000, v70
	v_max_f32_e32 v2, 0, v2
	v_fma_mixlo_f16 v3, v2, s6, 0
	v_mul_f32_e32 v19, 0x41800000, v2
	v_fma_mixlo_f16 v18, v2, s6, -v3 op_sel_hi:[0,0,1]
	v_fmamk_f32 v2, v55, 0x3a800000, v71
	v_max_f32_e32 v50, 0, v2
	v_fmamk_f32 v2, v56, 0x3a800000, v72
	v_max_f32_e32 v20, 0, v2
	global_load_dwordx4 v[2:5], v139, s[10:11] offset:192
	v_fmamk_f32 v21, v57, 0x3a800000, v73
	v_max_f32_e32 v21, 0, v21
	v_pk_mul_f32 v[34:35], v[20:21], s[6:7] op_sel_hi:[1,0]
	v_mul_f32_e32 v51, 0x41800000, v50
	v_cvt_pk_f16_f32 v35, v34, v35
	v_cvt_f32_f16_e32 v36, v35
	v_cvt_f32_f16_sdwa v37, v35 dst_sel:DWORD dst_unused:UNUSED_PAD src0_sel:WORD_1
	v_fma_mixlo_f16 v52, v50, s6, 0
	v_cvt_pk_f16_f32 v34, v19, v51
	v_fma_mixhi_f16 v18, v50, s6, -v52 op_sel_hi:[0,0,1]
	v_pk_fma_f32 v[20:21], v[20:21], s[6:7], v[36:37] op_sel_hi:[1,0,1] neg_lo:[0,0,1] neg_hi:[0,0,1]
	v_fmamk_f32 v6, v6, 0x3a800000, v70
	v_cvt_pk_f16_f32 v19, v20, v21
	ds_write2_b64 v138, v[34:35], v[18:19] offset0:20 offset1:22
	v_fmamk_f32 v18, v38, 0x3a800000, v70
	v_max_f32_e32 v18, 0, v18
	v_fma_mixlo_f16 v20, v18, s6, 0
	v_mul_f32_e32 v19, 0x41800000, v18
	v_fma_mixlo_f16 v18, v18, s6, -v20 op_sel_hi:[0,0,1]
	v_fmamk_f32 v20, v39, 0x3a800000, v71
	v_max_f32_e32 v38, 0, v20
	v_fmamk_f32 v20, v40, 0x3a800000, v72
	v_fmamk_f32 v21, v41, 0x3a800000, v73
	v_max_f32_e32 v20, 0, v20
	v_max_f32_e32 v21, 0, v21
	v_pk_mul_f32 v[34:35], v[20:21], s[6:7] op_sel_hi:[1,0]
	v_mul_f32_e32 v39, 0x41800000, v38
	v_cvt_pk_f16_f32 v35, v34, v35
	v_cvt_f32_f16_e32 v36, v35
	v_cvt_f32_f16_sdwa v37, v35 dst_sel:DWORD dst_unused:UNUSED_PAD src0_sel:WORD_1
	v_fma_mixlo_f16 v40, v38, s6, 0
	v_cvt_pk_f16_f32 v34, v19, v39
	v_fma_mixhi_f16 v18, v38, s6, -v40 op_sel_hi:[0,0,1]
	v_pk_fma_f32 v[20:21], v[20:21], s[6:7], v[36:37] op_sel_hi:[1,0,1] neg_lo:[0,0,1] neg_hi:[0,0,1]
	v_max_f32_e32 v6, 0, v6
	v_cvt_pk_f16_f32 v19, v20, v21
	ds_write2_b64 v137, v[34:35], v[18:19] offset0:84 offset1:86
	v_fmamk_f32 v18, v22, 0x3a800000, v70
	v_max_f32_e32 v18, 0, v18
	v_fma_mixlo_f16 v20, v18, s6, 0
	v_mul_f32_e32 v19, 0x41800000, v18
	v_fma_mixlo_f16 v18, v18, s6, -v20 op_sel_hi:[0,0,1]
	v_fmamk_f32 v20, v23, 0x3a800000, v71
	v_max_f32_e32 v34, 0, v20
	v_fmamk_f32 v20, v24, 0x3a800000, v72
	v_fmamk_f32 v21, v25, 0x3a800000, v73
	v_max_f32_e32 v20, 0, v20
	v_max_f32_e32 v21, 0, v21
	v_pk_mul_f32 v[22:23], v[20:21], s[6:7] op_sel_hi:[1,0]
	v_mul_f32_e32 v35, 0x41800000, v34
	v_cvt_pk_f16_f32 v23, v22, v23
	v_cvt_f32_f16_e32 v24, v23
	v_cvt_f32_f16_sdwa v25, v23 dst_sel:DWORD dst_unused:UNUSED_PAD src0_sel:WORD_1
	v_fma_mixlo_f16 v36, v34, s6, 0
	v_cvt_pk_f16_f32 v22, v19, v35
	v_fma_mixhi_f16 v18, v34, s6, -v36 op_sel_hi:[0,0,1]
	v_pk_fma_f32 v[20:21], v[20:21], s[6:7], v[24:25] op_sel_hi:[1,0,1] neg_lo:[0,0,1] neg_hi:[0,0,1]
	v_fmamk_f32 v8, v8, 0x3a800000, v72
	v_cvt_pk_f16_f32 v19, v20, v21
	v_fmac_f32_e32 v73, 0x3a800000, v9
	ds_write2_b64 v136, v[22:23], v[18:19] offset0:148 offset1:150
	v_fma_mixlo_f16 v18, v6, s6, 0
	v_max_f32_e32 v8, 0, v8
	v_max_f32_e32 v9, 0, v73
	v_mul_f32_e32 v22, 0x41800000, v6
	v_fma_mixlo_f16 v6, v6, s6, -v18 op_sel_hi:[0,0,1]
	v_pk_mul_f32 v[18:19], v[8:9], s[6:7] op_sel_hi:[1,0]
	v_fmamk_f32 v7, v7, 0x3a800000, v71
	v_cvt_pk_f16_f32 v19, v18, v19
	v_cvt_f32_f16_e32 v20, v19
	v_cvt_f32_f16_sdwa v21, v19 dst_sel:DWORD dst_unused:UNUSED_PAD src0_sel:WORD_1
	v_max_f32_e32 v7, 0, v7
	v_mul_f32_e32 v23, 0x41800000, v7
	v_fma_mixlo_f16 v24, v7, s6, 0
	v_pk_fma_f32 v[8:9], v[8:9], s[6:7], v[20:21] op_sel_hi:[1,0,1] neg_lo:[0,0,1] neg_hi:[0,0,1]
	v_cvt_pk_f16_f32 v18, v22, v23
	v_fma_mixhi_f16 v6, v7, s6, -v24 op_sel_hi:[0,0,1]
	v_cvt_pk_f16_f32 v7, v8, v9
	ds_write2_b64 v82, v[18:19], v[6:7] offset0:212 offset1:214
	global_load_dwordx4 v[6:9], v139, s[10:11] offset:224
	s_waitcnt vmcnt(1)
	v_fmamk_f32 v18, v58, 0x3a800000, v2
	v_max_f32_e32 v18, 0, v18
	v_fma_mixlo_f16 v20, v18, s6, 0
	v_mul_f32_e32 v19, 0x41800000, v18
	v_fma_mixlo_f16 v18, v18, s6, -v20 op_sel_hi:[0,0,1]
	v_fmamk_f32 v20, v59, 0x3a800000, v3
	v_max_f32_e32 v34, 0, v20
	v_fmamk_f32 v20, v60, 0x3a800000, v4
	v_fmamk_f32 v21, v61, 0x3a800000, v5
	v_max_f32_e32 v20, 0, v20
	v_max_f32_e32 v21, 0, v21
	v_pk_mul_f32 v[22:23], v[20:21], s[6:7] op_sel_hi:[1,0]
	v_mul_f32_e32 v35, 0x41800000, v34
	v_cvt_pk_f16_f32 v23, v22, v23
	v_cvt_f32_f16_e32 v24, v23
	v_cvt_f32_f16_sdwa v25, v23 dst_sel:DWORD dst_unused:UNUSED_PAD src0_sel:WORD_1
	v_fma_mixlo_f16 v36, v34, s6, 0
	v_cvt_pk_f16_f32 v22, v19, v35
	v_fma_mixhi_f16 v18, v34, s6, -v36 op_sel_hi:[0,0,1]
	v_pk_fma_f32 v[20:21], v[20:21], s[6:7], v[24:25] op_sel_hi:[1,0,1] neg_lo:[0,0,1] neg_hi:[0,0,1]
	s_nop 0
	v_cvt_pk_f16_f32 v19, v20, v21
	ds_write2_b64 v138, v[22:23], v[18:19] offset0:24 offset1:26
	v_fmamk_f32 v18, v42, 0x3a800000, v2
	v_max_f32_e32 v18, 0, v18
	v_fma_mixlo_f16 v20, v18, s6, 0
	v_mul_f32_e32 v19, 0x41800000, v18
	v_fma_mixlo_f16 v18, v18, s6, -v20 op_sel_hi:[0,0,1]
	v_fmamk_f32 v20, v43, 0x3a800000, v3
	v_max_f32_e32 v34, 0, v20
	v_fmamk_f32 v20, v44, 0x3a800000, v4
	v_fmamk_f32 v21, v45, 0x3a800000, v5
	v_max_f32_e32 v20, 0, v20
	v_max_f32_e32 v21, 0, v21
	v_pk_mul_f32 v[22:23], v[20:21], s[6:7] op_sel_hi:[1,0]
	v_mul_f32_e32 v35, 0x41800000, v34
	v_cvt_pk_f16_f32 v23, v22, v23
	v_cvt_f32_f16_e32 v24, v23
	v_cvt_f32_f16_sdwa v25, v23 dst_sel:DWORD dst_unused:UNUSED_PAD src0_sel:WORD_1
	v_fma_mixlo_f16 v36, v34, s6, 0
	v_cvt_pk_f16_f32 v22, v19, v35
	v_fma_mixhi_f16 v18, v34, s6, -v36 op_sel_hi:[0,0,1]
	v_pk_fma_f32 v[20:21], v[20:21], s[6:7], v[24:25] op_sel_hi:[1,0,1] neg_lo:[0,0,1] neg_hi:[0,0,1]
	s_nop 0
	v_cvt_pk_f16_f32 v19, v20, v21
	ds_write2_b64 v137, v[22:23], v[18:19] offset0:88 offset1:90
	v_fmamk_f32 v18, v26, 0x3a800000, v2
	v_max_f32_e32 v18, 0, v18
	v_fma_mixlo_f16 v20, v18, s6, 0
	v_mul_f32_e32 v19, 0x41800000, v18
	v_fma_mixlo_f16 v18, v18, s6, -v20 op_sel_hi:[0,0,1]
	v_fmamk_f32 v20, v27, 0x3a800000, v3
	v_max_f32_e32 v26, 0, v20
	v_fmamk_f32 v20, v28, 0x3a800000, v4
	v_fmamk_f32 v21, v29, 0x3a800000, v5
	v_max_f32_e32 v20, 0, v20
	v_max_f32_e32 v21, 0, v21
	v_pk_mul_f32 v[22:23], v[20:21], s[6:7] op_sel_hi:[1,0]
	v_fmamk_f32 v2, v10, 0x3a800000, v2
	v_cvt_pk_f16_f32 v23, v22, v23
	v_cvt_f32_f16_e32 v24, v23
	v_cvt_f32_f16_sdwa v25, v23 dst_sel:DWORD dst_unused:UNUSED_PAD src0_sel:WORD_1
	v_mul_f32_e32 v27, 0x41800000, v26
	v_fma_mixlo_f16 v28, v26, s6, 0
	v_max_f32_e32 v2, 0, v2
	v_pk_fma_f32 v[20:21], v[20:21], s[6:7], v[24:25] op_sel_hi:[1,0,1] neg_lo:[0,0,1] neg_hi:[0,0,1]
	v_fmamk_f32 v4, v12, 0x3a800000, v4
	v_fmac_f32_e32 v5, 0x3a800000, v13
	v_cvt_pk_f16_f32 v22, v19, v27
	v_fma_mixhi_f16 v18, v26, s6, -v28 op_sel_hi:[0,0,1]
	v_cvt_pk_f16_f32 v19, v20, v21
	v_fma_mixlo_f16 v10, v2, s6, 0
	v_max_f32_e32 v4, 0, v4
	v_max_f32_e32 v5, 0, v5
	ds_write2_b64 v136, v[22:23], v[18:19] offset0:152 offset1:154
	v_mul_f32_e32 v18, 0x41800000, v2
	v_fma_mixlo_f16 v2, v2, s6, -v10 op_sel_hi:[0,0,1]
	v_fmamk_f32 v3, v11, 0x3a800000, v3
	v_pk_mul_f32 v[10:11], v[4:5], s[6:7] op_sel_hi:[1,0]
	v_max_f32_e32 v3, 0, v3
	v_cvt_pk_f16_f32 v11, v10, v11
	v_cvt_f32_f16_e32 v12, v11
	v_cvt_f32_f16_sdwa v13, v11 dst_sel:DWORD dst_unused:UNUSED_PAD src0_sel:WORD_1
	v_mul_f32_e32 v19, 0x41800000, v3
	v_fma_mixlo_f16 v20, v3, s6, 0
	v_cvt_pk_f16_f32 v10, v18, v19
	v_pk_fma_f32 v[4:5], v[4:5], s[6:7], v[12:13] op_sel_hi:[1,0,1] neg_lo:[0,0,1] neg_hi:[0,0,1]
	v_fma_mixhi_f16 v2, v3, s6, -v20 op_sel_hi:[0,0,1]
	v_cvt_pk_f16_f32 v3, v4, v5
	ds_write2_b64 v82, v[10:11], v[2:3] offset0:216 offset1:218
	s_waitcnt vmcnt(0)
	v_fmamk_f32 v2, v62, 0x3a800000, v6
	v_max_f32_e32 v2, 0, v2
	v_fma_mixlo_f16 v4, v2, s6, 0
	v_mul_f32_e32 v3, 0x41800000, v2
	v_fma_mixlo_f16 v2, v2, s6, -v4 op_sel_hi:[0,0,1]
	v_fmamk_f32 v4, v63, 0x3a800000, v7
	v_max_f32_e32 v18, 0, v4
	v_fmamk_f32 v4, v64, 0x3a800000, v8
	v_fmamk_f32 v5, v65, 0x3a800000, v9
	v_max_f32_e32 v4, 0, v4
	v_max_f32_e32 v5, 0, v5
	v_pk_mul_f32 v[10:11], v[4:5], s[6:7] op_sel_hi:[1,0]
	v_mul_f32_e32 v19, 0x41800000, v18
	v_cvt_pk_f16_f32 v11, v10, v11
	v_cvt_f32_f16_e32 v12, v11
	v_cvt_f32_f16_sdwa v13, v11 dst_sel:DWORD dst_unused:UNUSED_PAD src0_sel:WORD_1
	v_fma_mixlo_f16 v20, v18, s6, 0
	v_cvt_pk_f16_f32 v10, v3, v19
	v_fma_mixhi_f16 v2, v18, s6, -v20 op_sel_hi:[0,0,1]
	v_pk_fma_f32 v[4:5], v[4:5], s[6:7], v[12:13] op_sel_hi:[1,0,1] neg_lo:[0,0,1] neg_hi:[0,0,1]
	s_nop 0
	v_cvt_pk_f16_f32 v3, v4, v5
	ds_write2_b64 v138, v[10:11], v[2:3] offset0:28 offset1:30
	v_fmamk_f32 v2, v46, 0x3a800000, v6
	v_max_f32_e32 v2, 0, v2
	v_fma_mixlo_f16 v4, v2, s6, 0
	v_mul_f32_e32 v3, 0x41800000, v2
	v_fma_mixlo_f16 v2, v2, s6, -v4 op_sel_hi:[0,0,1]
	v_fmamk_f32 v4, v47, 0x3a800000, v7
	v_max_f32_e32 v18, 0, v4
	v_fmamk_f32 v4, v48, 0x3a800000, v8
	v_fmamk_f32 v5, v49, 0x3a800000, v9
	v_max_f32_e32 v4, 0, v4
	v_max_f32_e32 v5, 0, v5
	v_pk_mul_f32 v[10:11], v[4:5], s[6:7] op_sel_hi:[1,0]
	v_mul_f32_e32 v19, 0x41800000, v18
	v_cvt_pk_f16_f32 v11, v10, v11
	v_cvt_f32_f16_e32 v12, v11
	v_cvt_f32_f16_sdwa v13, v11 dst_sel:DWORD dst_unused:UNUSED_PAD src0_sel:WORD_1
	v_fma_mixlo_f16 v20, v18, s6, 0
	v_cvt_pk_f16_f32 v10, v3, v19
	v_fma_mixhi_f16 v2, v18, s6, -v20 op_sel_hi:[0,0,1]
	v_pk_fma_f32 v[4:5], v[4:5], s[6:7], v[12:13] op_sel_hi:[1,0,1] neg_lo:[0,0,1] neg_hi:[0,0,1]
	s_nop 0
	v_cvt_pk_f16_f32 v3, v4, v5
	ds_write2_b64 v137, v[10:11], v[2:3] offset0:92 offset1:94
	v_fmamk_f32 v2, v30, 0x3a800000, v6
	v_max_f32_e32 v2, 0, v2
	v_fma_mixlo_f16 v4, v2, s6, 0
	v_mul_f32_e32 v3, 0x41800000, v2
	v_fma_mixlo_f16 v2, v2, s6, -v4 op_sel_hi:[0,0,1]
	v_fmamk_f32 v4, v31, 0x3a800000, v7
	v_max_f32_e32 v18, 0, v4
	v_fmamk_f32 v4, v32, 0x3a800000, v8
	v_fmamk_f32 v5, v33, 0x3a800000, v9
	v_max_f32_e32 v4, 0, v4
	v_max_f32_e32 v5, 0, v5
	v_pk_mul_f32 v[10:11], v[4:5], s[6:7] op_sel_hi:[1,0]
	v_mul_f32_e32 v19, 0x41800000, v18
	v_cvt_pk_f16_f32 v11, v10, v11
	v_cvt_f32_f16_e32 v12, v11
	v_cvt_f32_f16_sdwa v13, v11 dst_sel:DWORD dst_unused:UNUSED_PAD src0_sel:WORD_1
	v_fma_mixlo_f16 v20, v18, s6, 0
	v_cvt_pk_f16_f32 v10, v3, v19
	v_fma_mixhi_f16 v2, v18, s6, -v20 op_sel_hi:[0,0,1]
	v_pk_fma_f32 v[4:5], v[4:5], s[6:7], v[12:13] op_sel_hi:[1,0,1] neg_lo:[0,0,1] neg_hi:[0,0,1]
	v_fmac_f32_e32 v9, 0x3a800000, v17
	v_cvt_pk_f16_f32 v3, v4, v5
	ds_write2_b64 v136, v[10:11], v[2:3] offset0:156 offset1:158
	v_fmamk_f32 v2, v14, 0x3a800000, v6
	v_max_f32_e32 v2, 0, v2
	v_fma_mixlo_f16 v4, v2, s6, 0
	v_mul_f32_e32 v3, 0x41800000, v2
	v_fma_mixlo_f16 v2, v2, s6, -v4 op_sel_hi:[0,0,1]
	v_fmamk_f32 v4, v15, 0x3a800000, v7
	v_max_f32_e32 v10, 0, v4
	v_fmamk_f32 v4, v16, 0x3a800000, v8
	v_max_f32_e32 v4, 0, v4
	v_max_f32_e32 v5, 0, v9
	v_pk_mul_f32 v[6:7], v[4:5], s[6:7] op_sel_hi:[1,0]
	v_mul_f32_e32 v11, 0x41800000, v10
	v_cvt_pk_f16_f32 v7, v6, v7
	v_cvt_f32_f16_e32 v8, v7
	v_cvt_f32_f16_sdwa v9, v7 dst_sel:DWORD dst_unused:UNUSED_PAD src0_sel:WORD_1
	v_fma_mixlo_f16 v12, v10, s6, 0
	v_cvt_pk_f16_f32 v6, v3, v11
	v_fma_mixhi_f16 v2, v10, s6, -v12 op_sel_hi:[0,0,1]
	v_pk_fma_f32 v[4:5], v[4:5], s[6:7], v[8:9] op_sel_hi:[1,0,1] neg_lo:[0,0,1] neg_hi:[0,0,1]
	s_mov_b64 s[6:7], 0
	v_cvt_pk_f16_f32 v3, v4, v5
	ds_write2_b64 v82, v[6:7], v[2:3] offset0:220 offset1:222
	s_branch .LBB5_5
